# hot loop heads (GEMM K-loops, attention steady loop) aligned to 64 bytes
# speedup vs baseline: 1.0055x; 1.0055x over previous
.LBB0_469:
	s_ashr_i32 s7, s6, 31
	s_lshl_b64 s[8:9], s[6:7], 19
	s_add_u32 s8, s96, s8
	s_addc_u32 s9, s97, s9
	s_ashr_i32 s5, s4, 31
	s_lshl_b64 s[10:11], s[4:5], 19
	s_add_u32 s10, s17, s10
	s_addc_u32 s11, s25, s11
	s_add_u32 s18, s34, 0x100
	s_addc_u32 s19, s35, 0
	s_add_u32 s42, s34, 0x180
	s_addc_u32 s43, s35, 0
	s_add_u32 s46, s30, 0x100
	s_addc_u32 s47, s31, 0
	s_add_i32 s61, 0, 0x10000
	s_add_i32 s52, 0, 0x14000
	v_add_u32_e32 v134, s61, v146
	v_add_u32_e32 v135, s52, v146
	ds_read_b128 v[2:5], v134
	ds_read_b128 v[6:9], v134 offset:1024
	ds_read_b128 v[10:13], v134 offset:2048
	ds_read_b128 v[14:17], v134 offset:3072
	ds_read_b128 v[18:21], v135
	ds_read_b128 v[22:25], v135 offset:1024
	ds_read_b128 v[26:29], v135 offset:2048
	ds_read_b128 v[30:33], v135 offset:3072
	s_mov_b64 s[40:41], 0x100
	s_add_u32 s50, s34, 0x40080
	s_addc_u32 s51, s35, 0
	s_add_i32 s5, s23, 0xc000
	ds_read_b128 v[34:37], v149
	ds_read_b128 v[38:41], v149 offset:1024
	ds_read_b128 v[42:45], v149 offset:2048
	ds_read_b128 v[46:49], v149 offset:3072
	ds_read_b128 v[50:53], v149 offset:4096
	ds_read_b128 v[54:57], v149 offset:5120
	ds_read_b128 v[58:61], v149 offset:6144
	ds_read_b128 v[62:65], v149 offset:7168
	s_mov_b32 m0, s5
	v_lshl_add_u64 v[66:67], s[50:51], 0, v[132:133]
	s_add_i32 s7, s23, 0xe000
	global_load_lds_dwordx4 v[66:67], off
	v_lshl_add_u64 v[66:67], s[50:51], 0, v[130:131]
	s_mov_b32 m0, s7
	s_nop 0
	global_load_lds_dwordx4 v[66:67], off
	s_waitcnt vmcnt(8)
	s_waitcnt lgkmcnt(0)
	s_barrier
	s_setprio 1
	s_waitcnt lgkmcnt(0)
	v_mfma_f32_16x16x32_bf16 v[86:89], v[10:13], v[50:53], 0
	v_mfma_f32_16x16x32_bf16 v[90:93], v[14:17], v[54:57], v[86:89]
	v_mfma_f32_16x16x32_bf16 v[86:89], v[2:5], v[58:61], 0
	v_mfma_f32_16x16x32_bf16 v[66:69], v[2:5], v[34:37], 0
	v_mfma_f32_16x16x32_bf16 v[70:73], v[10:13], v[34:37], 0
	v_mfma_f32_16x16x32_bf16 v[74:77], v[2:5], v[42:45], 0
	v_mfma_f32_16x16x32_bf16 v[78:81], v[10:13], v[42:45], 0
	v_mfma_f32_16x16x32_bf16 v[82:85], v[2:5], v[50:53], 0
	v_mfma_f32_16x16x32_bf16 v[94:97], v[6:9], v[62:65], v[86:89]
	v_mfma_f32_16x16x32_bf16 v[86:89], v[10:13], v[58:61], 0
	v_mfma_f32_16x16x32_bf16 v[66:69], v[6:9], v[38:41], v[66:69]
	v_mfma_f32_16x16x32_bf16 v[70:73], v[14:17], v[38:41], v[70:73]
	v_mfma_f32_16x16x32_bf16 v[74:77], v[6:9], v[46:49], v[74:77]
	v_mfma_f32_16x16x32_bf16 v[78:81], v[14:17], v[46:49], v[78:81]
	v_mfma_f32_16x16x32_bf16 v[82:85], v[6:9], v[54:57], v[82:85]
	v_mfma_f32_16x16x32_bf16 v[102:105], v[14:17], v[62:65], v[86:89]
	s_setprio 0
	s_setprio 1
	v_mfma_f32_16x16x32_bf16 v[86:89], v[18:21], v[34:37], 0
	v_mfma_f32_16x16x32_bf16 v[34:37], v[26:29], v[34:37], 0
	v_mfma_f32_16x16x32_bf16 v[110:113], v[22:25], v[38:41], v[86:89]
	v_mfma_f32_16x16x32_bf16 v[34:37], v[30:33], v[38:41], v[34:37]
	v_mfma_f32_16x16x32_bf16 v[38:41], v[18:21], v[42:45], 0
	v_mfma_f32_16x16x32_bf16 v[138:141], v[22:25], v[46:49], v[38:41]
	v_mfma_f32_16x16x32_bf16 v[38:41], v[26:29], v[42:45], 0
	v_mfma_f32_16x16x32_bf16 v[42:45], v[30:33], v[46:49], v[38:41]
	v_mfma_f32_16x16x32_bf16 v[38:41], v[18:21], v[50:53], 0
	v_mfma_f32_16x16x32_bf16 v[46:49], v[22:25], v[54:57], v[38:41]
	v_mfma_f32_16x16x32_bf16 v[38:41], v[26:29], v[50:53], 0
	v_mfma_f32_16x16x32_bf16 v[50:53], v[30:33], v[54:57], v[38:41]
	v_mfma_f32_16x16x32_bf16 v[38:41], v[18:21], v[58:61], 0
	v_mfma_f32_16x16x32_bf16 v[142:145], v[22:25], v[62:65], v[38:41]
	v_mfma_f32_16x16x32_bf16 v[38:41], v[26:29], v[58:61], 0
	v_mfma_f32_16x16x32_bf16 v[58:61], v[30:33], v[62:65], v[38:41]
	s_setprio 0
	s_barrier
	s_add_i32 s61, s61, s33
	s_nop 3
	ds_read_b128 v[38:41], v149 offset:16384
	ds_read_b128 v[54:57], v149 offset:17408
	ds_read_b128 v[62:65], v149 offset:18432
	ds_read_b128 v[86:89], v149 offset:19456
	ds_read_b128 v[98:101], v149 offset:20480
	ds_read_b128 v[106:109], v149 offset:21504
	ds_read_b128 v[114:117], v149 offset:22528
	ds_read_b128 v[118:121], v149 offset:23552
	s_mov_b32 m0, s61
	v_lshl_add_u64 v[122:123], s[46:47], 0, v[132:133]
	global_load_lds_dwordx4 v[122:123], off
	v_lshl_add_u64 v[122:123], s[46:47], 0, v[130:131]
	s_add_i32 s46, s61, 0x2000
	s_add_u32 s50, s30, 0x40100
	s_mov_b32 m0, s46
	s_addc_u32 s51, s31, 0
	s_add_i32 s47, s52, s33
	global_load_lds_dwordx4 v[122:123], off
	s_mov_b32 m0, s47
	v_lshl_add_u64 v[122:123], s[50:51], 0, v[132:133]
	s_add_i32 s62, s47, 0x2000
	global_load_lds_dwordx4 v[122:123], off
	v_lshl_add_u64 v[122:123], s[50:51], 0, v[130:131]
	s_mov_b32 m0, s62
	s_nop 0
	global_load_lds_dwordx4 v[122:123], off
	s_mov_b32 m0, s23
	v_lshl_add_u64 v[122:123], s[18:19], 0, v[132:133]
	global_load_lds_dwordx4 v[122:123], off
	v_lshl_add_u64 v[122:123], s[18:19], 0, v[130:131]
	s_mov_b32 m0, s29
	s_nop 0
	global_load_lds_dwordx4 v[122:123], off
	s_waitcnt vmcnt(8)
	s_waitcnt lgkmcnt(0)
	s_barrier
	s_setprio 1
	s_waitcnt lgkmcnt(0)
	v_mfma_f32_16x16x32_bf16 v[122:125], v[2:5], v[38:41], 0
	v_mfma_f32_16x16x32_bf16 v[150:153], v[6:9], v[54:57], v[122:125]
	v_mfma_f32_16x16x32_bf16 v[122:125], v[10:13], v[38:41], 0
	v_mfma_f32_16x16x32_bf16 v[154:157], v[14:17], v[54:57], v[122:125]
	v_mfma_f32_16x16x32_bf16 v[122:125], v[2:5], v[62:65], 0
	v_mfma_f32_16x16x32_bf16 v[158:161], v[6:9], v[86:89], v[122:125]
	v_mfma_f32_16x16x32_bf16 v[122:125], v[10:13], v[62:65], 0
	v_mfma_f32_16x16x32_bf16 v[162:165], v[14:17], v[86:89], v[122:125]
	v_mfma_f32_16x16x32_bf16 v[122:125], v[2:5], v[98:101], 0
	v_mfma_f32_16x16x32_bf16 v[2:5], v[2:5], v[114:117], 0
	v_mfma_f32_16x16x32_bf16 v[166:169], v[6:9], v[106:109], v[122:125]
	v_mfma_f32_16x16x32_bf16 v[2:5], v[6:9], v[118:121], v[2:5]
	v_mfma_f32_16x16x32_bf16 v[6:9], v[10:13], v[114:117], 0
	v_mfma_f32_16x16x32_bf16 v[122:125], v[10:13], v[98:101], 0
	v_mfma_f32_16x16x32_bf16 v[6:9], v[14:17], v[118:121], v[6:9]
	v_mfma_f32_16x16x32_bf16 v[170:173], v[14:17], v[106:109], v[122:125]
	s_setprio 0
	s_setprio 1
	v_mfma_f32_16x16x32_bf16 v[10:13], v[18:21], v[38:41], 0
	v_mfma_f32_16x16x32_bf16 v[174:177], v[22:25], v[54:57], v[10:13]
	v_mfma_f32_16x16x32_bf16 v[10:13], v[26:29], v[38:41], 0
	v_mfma_f32_16x16x32_bf16 v[178:181], v[30:33], v[54:57], v[10:13]
	v_mfma_f32_16x16x32_bf16 v[10:13], v[18:21], v[62:65], 0
	v_mfma_f32_16x16x32_bf16 v[182:185], v[22:25], v[86:89], v[10:13]
	v_mfma_f32_16x16x32_bf16 v[10:13], v[26:29], v[62:65], 0
	v_mfma_f32_16x16x32_bf16 v[186:189], v[30:33], v[86:89], v[10:13]
	v_mfma_f32_16x16x32_bf16 v[10:13], v[18:21], v[98:101], 0
	v_mfma_f32_16x16x32_bf16 v[194:197], v[22:25], v[106:109], v[10:13]
	v_mfma_f32_16x16x32_bf16 v[10:13], v[26:29], v[98:101], 0
	v_mfma_f32_16x16x32_bf16 v[198:201], v[30:33], v[106:109], v[10:13]
	v_mfma_f32_16x16x32_bf16 v[10:13], v[18:21], v[114:117], 0
	v_mfma_f32_16x16x32_bf16 v[202:205], v[22:25], v[118:121], v[10:13]
	v_mfma_f32_16x16x32_bf16 v[10:13], v[26:29], v[114:117], 0
	v_mfma_f32_16x16x32_bf16 v[214:217], v[30:33], v[118:121], v[10:13]
	s_setprio 0
	s_barrier
	s_add_i32 s63, 0, 0x18000
	s_add_i32 s65, 0, 0x1c000
	v_add_u32_e32 v136, s63, v146
	v_add_u32_e32 v137, s65, v146
	s_nop 0
	ds_read_b128 v[10:13], v136
	ds_read_b128 v[14:17], v136 offset:1024
	ds_read_b128 v[18:21], v136 offset:2048
	ds_read_b128 v[22:25], v136 offset:3072
	ds_read_b128 v[218:221], v137
	ds_read_b128 v[222:225], v137 offset:1024
	ds_read_b128 v[226:229], v137 offset:2048
	ds_read_b128 v[230:233], v137 offset:3072
	s_add_u32 s18, s34, 0x40100
	s_addc_u32 s19, s35, 0
	s_mov_b32 m0, s55
	ds_read_b128 v[26:29], v149 offset:32768
	ds_read_b128 v[30:33], v149 offset:33792
	ds_read_b128 v[62:65], v149 offset:34816
	ds_read_b128 v[234:237], v149 offset:35840
	ds_read_b128 v[238:241], v149 offset:36864
	ds_read_b128 v[242:245], v149 offset:37888
	ds_read_b128 v[246:249], v149 offset:38912
	ds_read_b128 v[206:209], v149 offset:39936
	s_nop 0
	v_lshl_add_u64 v[38:39], s[18:19], 0, v[132:133]
	global_load_lds_dwordx4 v[38:39], off
	v_lshl_add_u64 v[38:39], s[18:19], 0, v[130:131]
	s_mov_b32 m0, s56
	s_nop 0
	global_load_lds_dwordx4 v[38:39], off
	s_waitcnt vmcnt(8)
	s_waitcnt lgkmcnt(0)
	s_barrier
	s_setprio 1
	s_waitcnt lgkmcnt(0)
	v_mfma_f32_16x16x32_bf16 v[38:41], v[10:13], v[26:29], v[66:69]
	v_mfma_f32_16x16x32_bf16 v[122:125], v[14:17], v[30:33], v[38:41]
	v_mfma_f32_16x16x32_bf16 v[38:41], v[18:21], v[26:29], v[70:73]
	v_mfma_f32_16x16x32_bf16 v[114:117], v[22:25], v[30:33], v[38:41]
	v_mfma_f32_16x16x32_bf16 v[38:41], v[10:13], v[62:65], v[74:77]
	v_mfma_f32_16x16x32_bf16 v[106:109], v[14:17], v[234:237], v[38:41]
	v_mfma_f32_16x16x32_bf16 v[38:41], v[18:21], v[62:65], v[78:81]
	v_mfma_f32_16x16x32_bf16 v[98:101], v[22:25], v[234:237], v[38:41]
	v_mfma_f32_16x16x32_bf16 v[38:41], v[10:13], v[238:241], v[82:85]
	v_mfma_f32_16x16x32_bf16 v[86:89], v[14:17], v[242:245], v[38:41]
	v_mfma_f32_16x16x32_bf16 v[38:41], v[18:21], v[238:241], v[90:93]
	v_mfma_f32_16x16x32_bf16 v[70:73], v[22:25], v[242:245], v[38:41]
	v_mfma_f32_16x16x32_bf16 v[38:41], v[10:13], v[246:249], v[94:97]
	v_mfma_f32_16x16x32_bf16 v[54:57], v[14:17], v[206:209], v[38:41]
	v_mfma_f32_16x16x32_bf16 v[38:41], v[18:21], v[246:249], v[102:105]
	v_mfma_f32_16x16x32_bf16 v[38:41], v[22:25], v[206:209], v[38:41]
	s_setprio 0
	s_setprio 1
	v_mfma_f32_16x16x32_bf16 v[66:69], v[218:221], v[26:29], v[110:113]
	v_mfma_f32_16x16x32_bf16 v[26:29], v[226:229], v[26:29], v[34:37]
	v_mfma_f32_16x16x32_bf16 v[118:121], v[230:233], v[30:33], v[26:29]
	v_mfma_f32_16x16x32_bf16 v[26:29], v[218:221], v[62:65], v[138:141]
	v_mfma_f32_16x16x32_bf16 v[110:113], v[222:225], v[234:237], v[26:29]
	v_mfma_f32_16x16x32_bf16 v[26:29], v[226:229], v[62:65], v[42:45]
	v_mfma_f32_16x16x32_bf16 v[102:105], v[230:233], v[234:237], v[26:29]
	v_mfma_f32_16x16x32_bf16 v[26:29], v[218:221], v[238:241], v[46:49]
	v_mfma_f32_16x16x32_bf16 v[90:93], v[222:225], v[242:245], v[26:29]
	v_mfma_f32_16x16x32_bf16 v[26:29], v[226:229], v[238:241], v[50:53]
	v_mfma_f32_16x16x32_bf16 v[74:77], v[230:233], v[242:245], v[26:29]
	v_mfma_f32_16x16x32_bf16 v[26:29], v[218:221], v[246:249], v[142:145]
	v_mfma_f32_16x16x32_bf16 v[62:65], v[222:225], v[206:209], v[26:29]
	v_mfma_f32_16x16x32_bf16 v[26:29], v[226:229], v[246:249], v[58:61]
	v_mfma_f32_16x16x32_bf16 v[126:129], v[222:225], v[30:33], v[66:69]
	v_mfma_f32_16x16x32_bf16 v[50:53], v[230:233], v[206:209], v[26:29]
	s_setprio 0
	s_barrier
;     ...
;         PG8_TRIP(0, true);
; #pragma unroll 1
;         for (int t = 2; t < nt; t += 2) PG8_TRIP(t, false);
	s_add_u32 s18, s30, 0x180
	s_addc_u32 s19, s31, 0
	s_add_i32 s63, s63, s33
	ds_read_b128 v[34:37], v149 offset:49152
	ds_read_b128 v[42:45], v149 offset:50176
	ds_read_b128 v[138:141], v149 offset:51200
	ds_read_b128 v[142:145], v149 offset:52224
	ds_read_b128 v[206:209], v149 offset:53248
	ds_read_b128 v[234:237], v149 offset:54272
	ds_read_b128 v[238:241], v149 offset:55296
	ds_read_b128 v[242:245], v149 offset:56320
	s_mov_b32 m0, s63
	v_lshl_add_u64 v[26:27], s[18:19], 0, v[132:133]
	s_add_i32 s64, s63, 0x2000
	global_load_lds_dwordx4 v[26:27], off
	v_lshl_add_u64 v[26:27], s[18:19], 0, v[130:131]
	s_add_u32 s18, s30, 0x40180
	s_mov_b32 m0, s64
	s_addc_u32 s19, s31, 0
	s_add_i32 s65, s65, s33
	global_load_lds_dwordx4 v[26:27], off
	s_mov_b32 m0, s65
	v_lshl_add_u64 v[26:27], s[18:19], 0, v[132:133]
	s_add_i32 s66, s65, 0x2000
	global_load_lds_dwordx4 v[26:27], off
	v_lshl_add_u64 v[26:27], s[18:19], 0, v[130:131]
	s_mov_b32 m0, s66
	s_nop 0
	global_load_lds_dwordx4 v[26:27], off
	s_mov_b32 m0, s57
	v_lshl_add_u64 v[26:27], s[42:43], 0, v[132:133]
	global_load_lds_dwordx4 v[26:27], off
	v_lshl_add_u64 v[26:27], s[42:43], 0, v[130:131]
	s_mov_b32 m0, s58
	s_nop 0
	global_load_lds_dwordx4 v[26:27], off
	s_waitcnt vmcnt(8)
	s_waitcnt lgkmcnt(0)
	s_barrier
	s_setprio 1
	s_waitcnt lgkmcnt(0)
	v_mfma_f32_16x16x32_bf16 v[26:29], v[10:13], v[34:37], v[150:153]
	v_mfma_f32_16x16x32_bf16 v[94:97], v[14:17], v[42:45], v[26:29]
	v_mfma_f32_16x16x32_bf16 v[26:29], v[18:21], v[34:37], v[154:157]
	v_mfma_f32_16x16x32_bf16 v[82:85], v[22:25], v[42:45], v[26:29]
	v_mfma_f32_16x16x32_bf16 v[26:29], v[10:13], v[138:141], v[158:161]
	v_mfma_f32_16x16x32_bf16 v[58:61], v[14:17], v[142:145], v[26:29]
	v_mfma_f32_16x16x32_bf16 v[26:29], v[18:21], v[138:141], v[162:165]
	v_mfma_f32_16x16x32_bf16 v[46:49], v[22:25], v[142:145], v[26:29]
	v_mfma_f32_16x16x32_bf16 v[26:29], v[10:13], v[206:209], v[166:169]
	v_mfma_f32_16x16x32_bf16 v[2:5], v[10:13], v[238:241], v[2:5]
	v_mfma_f32_16x16x32_bf16 v[30:33], v[14:17], v[234:237], v[26:29]
	v_mfma_f32_16x16x32_bf16 v[26:29], v[18:21], v[206:209], v[170:173]
	v_mfma_f32_16x16x32_bf16 v[14:17], v[14:17], v[242:245], v[2:5]
	v_mfma_f32_16x16x32_bf16 v[2:5], v[18:21], v[238:241], v[6:9]
	v_mfma_f32_16x16x32_bf16 v[26:29], v[22:25], v[234:237], v[26:29]
	v_mfma_f32_16x16x32_bf16 v[10:13], v[22:25], v[242:245], v[2:5]
	s_setprio 0
	s_setprio 1
	v_mfma_f32_16x16x32_bf16 v[2:5], v[218:221], v[34:37], v[174:177]
	v_mfma_f32_16x16x32_bf16 v[78:81], v[222:225], v[42:45], v[2:5]
	v_mfma_f32_16x16x32_bf16 v[2:5], v[226:229], v[34:37], v[178:181]
	v_mfma_f32_16x16x32_bf16 v[66:69], v[230:233], v[42:45], v[2:5]
	v_mfma_f32_16x16x32_bf16 v[2:5], v[218:221], v[138:141], v[182:185]
	v_mfma_f32_16x16x32_bf16 v[42:45], v[222:225], v[142:145], v[2:5]
	v_mfma_f32_16x16x32_bf16 v[2:5], v[226:229], v[138:141], v[186:189]
	v_mfma_f32_16x16x32_bf16 v[34:37], v[230:233], v[142:145], v[2:5]
	v_mfma_f32_16x16x32_bf16 v[2:5], v[218:221], v[206:209], v[194:197]
	v_mfma_f32_16x16x32_bf16 v[22:25], v[222:225], v[234:237], v[2:5]
	v_mfma_f32_16x16x32_bf16 v[2:5], v[226:229], v[206:209], v[198:201]
	v_mfma_f32_16x16x32_bf16 v[18:21], v[230:233], v[234:237], v[2:5]
	v_mfma_f32_16x16x32_bf16 v[2:5], v[218:221], v[238:241], v[202:205]
	v_mfma_f32_16x16x32_bf16 v[6:9], v[222:225], v[242:245], v[2:5]
	v_mfma_f32_16x16x32_bf16 v[2:5], v[226:229], v[238:241], v[214:217]
	v_mfma_f32_16x16x32_bf16 v[2:5], v[230:233], v[242:245], v[2:5]
	s_setprio 0
	s_barrier
	s_mov_b32 s67, 0
	.p2align 6

.LBB0_669:
	s_ashr_i32 s53, s52, 31
	s_lshl_b64 s[18:19], s[52:53], 18
	s_add_u32 s54, s96, s18
	s_addc_u32 s55, s97, s19
	s_ashr_i32 s35, s34, 31
	s_lshl_b64 s[18:19], s[34:35], 18
	s_add_u32 s56, s17, s18
	s_addc_u32 s57, s25, s19
	s_add_u32 s18, s28, 0x100
	s_addc_u32 s19, s29, 0
	s_add_u32 s38, s28, 0x180
	s_addc_u32 s39, s29, 0
	s_add_u32 s40, s8, 0x100
	s_addc_u32 s41, s9, 0
	s_add_i32 s12, 0, 0x10000
	s_add_i32 s53, 0, 0x14000
	v_add_u32_e32 v173, s12, v167
	v_add_u32_e32 v174, s53, v167
	ds_read_b128 v[2:5], v173
	ds_read_b128 v[6:9], v173 offset:1024
	ds_read_b128 v[10:13], v173 offset:2048
	ds_read_b128 v[14:17], v173 offset:3072
	ds_read_b128 v[18:21], v174
	ds_read_b128 v[22:25], v174 offset:1024
	ds_read_b128 v[26:29], v174 offset:2048
	ds_read_b128 v[30:33], v174 offset:3072
	s_mov_b64 s[30:31], 0x100
	s_add_u32 s42, s28, 0x20080
	s_addc_u32 s43, s29, 0
	s_add_i32 s3, s46, 0xc000
	ds_read_b128 v[34:37], v172
	ds_read_b128 v[38:41], v172 offset:1024
	ds_read_b128 v[42:45], v172 offset:2048
	ds_read_b128 v[46:49], v172 offset:3072
	ds_read_b128 v[50:53], v172 offset:4096
	ds_read_b128 v[54:57], v172 offset:5120
	ds_read_b128 v[58:61], v172 offset:6144
	ds_read_b128 v[62:65], v172 offset:7168
	s_mov_b32 m0, s3
	v_lshl_add_u64 v[66:67], s[42:43], 0, v[162:163]
	s_add_i32 s7, s46, 0xe000
	global_load_lds_dwordx4 v[66:67], off
	v_lshl_add_u64 v[66:67], s[42:43], 0, v[164:165]
	s_mov_b32 m0, s7
	s_nop 0
	global_load_lds_dwordx4 v[66:67], off
	s_waitcnt vmcnt(8)
	s_waitcnt lgkmcnt(0)
	s_barrier
	s_setprio 1
	s_waitcnt lgkmcnt(0)
	v_mfma_f32_16x16x128_f8f6f4 v[146:149], v[2:9], v[34:41], 0
	v_mfma_f32_16x16x128_f8f6f4 v[150:153], v[10:17], v[34:41], 0
	v_mfma_f32_16x16x128_f8f6f4 v[134:137], v[2:9], v[42:49], 0
	v_mfma_f32_16x16x128_f8f6f4 v[130:133], v[10:17], v[42:49], 0
	v_mfma_f32_16x16x128_f8f6f4 v[118:121], v[2:9], v[50:57], 0
	v_mfma_f32_16x16x128_f8f6f4 v[114:117], v[10:17], v[50:57], 0
	v_mfma_f32_16x16x128_f8f6f4 v[102:105], v[2:9], v[58:65], 0
	v_mfma_f32_16x16x128_f8f6f4 v[98:101], v[10:17], v[58:65], 0
	s_setprio 0
	s_setprio 1
	v_mfma_f32_16x16x128_f8f6f4 v[154:157], v[18:25], v[34:41], 0
	v_mfma_f32_16x16x128_f8f6f4 v[158:161], v[26:33], v[34:41], 0
	v_mfma_f32_16x16x128_f8f6f4 v[142:145], v[18:25], v[42:49], 0
	v_mfma_f32_16x16x128_f8f6f4 v[138:141], v[26:33], v[42:49], 0
	v_mfma_f32_16x16x128_f8f6f4 v[126:129], v[18:25], v[50:57], 0
	v_mfma_f32_16x16x128_f8f6f4 v[122:125], v[26:33], v[50:57], 0
	v_mfma_f32_16x16x128_f8f6f4 v[110:113], v[18:25], v[58:65], 0
	v_mfma_f32_16x16x128_f8f6f4 v[106:109], v[26:33], v[58:65], 0
	s_setprio 0
	s_barrier
	s_add_i32 s12, s12, s45
	ds_read_b128 v[74:77], v172 offset:16384
	ds_read_b128 v[78:81], v172 offset:17408
	ds_read_b128 v[176:179], v172 offset:18432
	ds_read_b128 v[180:183], v172 offset:19456
	ds_read_b128 v[194:197], v172 offset:20480
	ds_read_b128 v[198:201], v172 offset:21504
	ds_read_b128 v[214:217], v172 offset:22528
	ds_read_b128 v[218:221], v172 offset:23552
	s_mov_b32 m0, s12
	v_lshl_add_u64 v[34:35], s[40:41], 0, v[162:163]
	s_add_i32 s35, s12, 0x2000
	global_load_lds_dwordx4 v[34:35], off
	v_lshl_add_u64 v[34:35], s[40:41], 0, v[164:165]
	s_add_u32 s40, s8, 0x20100
	s_mov_b32 m0, s35
	s_addc_u32 s41, s9, 0
	s_add_i32 s53, s53, s45
	global_load_lds_dwordx4 v[34:35], off
	s_mov_b32 m0, s53
	v_lshl_add_u64 v[34:35], s[40:41], 0, v[162:163]
	s_add_i32 s69, s53, 0x2000
	global_load_lds_dwordx4 v[34:35], off
	v_lshl_add_u64 v[34:35], s[40:41], 0, v[164:165]
	s_mov_b32 m0, s69
	s_nop 0
	global_load_lds_dwordx4 v[34:35], off
	s_mov_b32 m0, s46
	v_lshl_add_u64 v[34:35], s[18:19], 0, v[162:163]
	global_load_lds_dwordx4 v[34:35], off
	v_lshl_add_u64 v[34:35], s[18:19], 0, v[164:165]
	s_mov_b32 m0, s47
	s_nop 0
	global_load_lds_dwordx4 v[34:35], off
	s_waitcnt vmcnt(8)
	s_waitcnt lgkmcnt(0)
	s_barrier
	s_setprio 1
	s_waitcnt lgkmcnt(0)
	v_mfma_f32_16x16x128_f8f6f4 v[86:89], v[2:9], v[74:81], 0
	v_mfma_f32_16x16x128_f8f6f4 v[82:85], v[10:17], v[74:81], 0
	v_mfma_f32_16x16x128_f8f6f4 v[70:73], v[2:9], v[176:183], 0
	v_mfma_f32_16x16x128_f8f6f4 v[66:69], v[10:17], v[176:183], 0
	v_mfma_f32_16x16x128_f8f6f4 v[58:61], v[2:9], v[194:201], 0
	v_mfma_f32_16x16x128_f8f6f4 v[50:53], v[10:17], v[194:201], 0
	v_mfma_f32_16x16x128_f8f6f4 v[46:49], v[2:9], v[214:221], 0
	v_mfma_f32_16x16x128_f8f6f4 v[38:41], v[10:17], v[214:221], 0
	s_setprio 0
	s_setprio 1
	v_mfma_f32_16x16x128_f8f6f4 v[94:97], v[18:25], v[74:81], 0
	v_mfma_f32_16x16x128_f8f6f4 v[90:93], v[26:33], v[74:81], 0
	v_mfma_f32_16x16x128_f8f6f4 v[78:81], v[18:25], v[176:183], 0
	v_mfma_f32_16x16x128_f8f6f4 v[74:77], v[26:33], v[176:183], 0
	v_mfma_f32_16x16x128_f8f6f4 v[62:65], v[18:25], v[194:201], 0
	v_mfma_f32_16x16x128_f8f6f4 v[54:57], v[26:33], v[194:201], 0
	v_mfma_f32_16x16x128_f8f6f4 v[42:45], v[18:25], v[214:221], 0
	v_mfma_f32_16x16x128_f8f6f4 v[34:37], v[26:33], v[214:221], 0
	s_setprio 0
	s_barrier
;     ...
;         PG8_TRIP(0, true);
; #pragma unroll 1
;         for (int t = 2; t < nt; t += 2) PG8_TRIP(t, false);
	s_add_i32 s42, 0, 0x18000
	s_add_i32 s70, 0, 0x1c000
	v_add_u32_e32 v175, s42, v167
	v_add_u32_e32 v176, s70, v167
	ds_read_b128 v[26:29], v175
	ds_read_b128 v[30:33], v175 offset:1024
	ds_read_b128 v[18:21], v175 offset:2048
	ds_read_b128 v[22:25], v175 offset:3072
	ds_read_b128 v[10:13], v176
	ds_read_b128 v[14:17], v176 offset:1024
	ds_read_b128 v[2:5], v176 offset:2048
	ds_read_b128 v[6:9], v176 offset:3072
	s_add_u32 s18, s28, 0x20100
	s_addc_u32 s19, s29, 0
	s_mov_b32 m0, s61
	ds_read_b128 v[178:181], v172 offset:32768
	ds_read_b128 v[182:185], v172 offset:33792
	ds_read_b128 v[194:197], v172 offset:34816
	ds_read_b128 v[198:201], v172 offset:35840
	ds_read_b128 v[214:217], v172 offset:36864
	ds_read_b128 v[218:221], v172 offset:37888
	ds_read_b128 v[222:225], v172 offset:38912
	ds_read_b128 v[226:229], v172 offset:39936
	s_nop 0
	v_lshl_add_u64 v[186:187], s[18:19], 0, v[162:163]
	global_load_lds_dwordx4 v[186:187], off
	v_lshl_add_u64 v[186:187], s[18:19], 0, v[164:165]
	s_mov_b32 m0, s62
	s_nop 0
	global_load_lds_dwordx4 v[186:187], off
	s_waitcnt vmcnt(8)
	s_waitcnt lgkmcnt(0)
	s_barrier
	s_setprio 1
	s_waitcnt lgkmcnt(0)
	v_mfma_f32_16x16x128_f8f6f4 v[146:149], v[26:33], v[178:185], v[146:149]
	v_mfma_f32_16x16x128_f8f6f4 v[150:153], v[18:25], v[178:185], v[150:153]
	v_mfma_f32_16x16x128_f8f6f4 v[134:137], v[26:33], v[194:201], v[134:137]
	v_mfma_f32_16x16x128_f8f6f4 v[130:133], v[18:25], v[194:201], v[130:133]
	v_mfma_f32_16x16x128_f8f6f4 v[118:121], v[26:33], v[214:221], v[118:121]
	v_mfma_f32_16x16x128_f8f6f4 v[114:117], v[18:25], v[214:221], v[114:117]
	v_mfma_f32_16x16x128_f8f6f4 v[102:105], v[26:33], v[222:229], v[102:105]
	v_mfma_f32_16x16x128_f8f6f4 v[98:101], v[18:25], v[222:229], v[98:101]
	s_setprio 0
	s_setprio 1
	v_mfma_f32_16x16x128_f8f6f4 v[154:157], v[10:17], v[178:185], v[154:157]
	v_mfma_f32_16x16x128_f8f6f4 v[158:161], v[2:9], v[178:185], v[158:161]
	v_mfma_f32_16x16x128_f8f6f4 v[142:145], v[10:17], v[194:201], v[142:145]
	v_mfma_f32_16x16x128_f8f6f4 v[138:141], v[2:9], v[194:201], v[138:141]
	v_mfma_f32_16x16x128_f8f6f4 v[126:129], v[10:17], v[214:221], v[126:129]
	v_mfma_f32_16x16x128_f8f6f4 v[122:125], v[2:9], v[214:221], v[122:125]
	v_mfma_f32_16x16x128_f8f6f4 v[110:113], v[10:17], v[222:229], v[110:113]
	v_mfma_f32_16x16x128_f8f6f4 v[106:109], v[2:9], v[222:229], v[106:109]
	s_setprio 0
	s_barrier
	s_add_u32 s40, s8, 0x180
	s_addc_u32 s41, s9, 0
	s_add_i32 s18, s42, s45
	ds_read_b128 v[178:181], v172 offset:49152
	ds_read_b128 v[182:185], v172 offset:50176
	ds_read_b128 v[194:197], v172 offset:51200
	ds_read_b128 v[198:201], v172 offset:52224
	ds_read_b128 v[214:217], v172 offset:53248
	ds_read_b128 v[218:221], v172 offset:54272
	ds_read_b128 v[222:225], v172 offset:55296
	ds_read_b128 v[226:229], v172 offset:56320
	s_mov_b32 m0, s18
	v_lshl_add_u64 v[186:187], s[40:41], 0, v[162:163]
	s_add_i32 s19, s18, 0x2000
	global_load_lds_dwordx4 v[186:187], off
	v_lshl_add_u64 v[186:187], s[40:41], 0, v[164:165]
	s_add_u32 s40, s8, 0x20180
	s_mov_b32 m0, s19
	s_addc_u32 s41, s9, 0
	s_add_i32 s70, s70, s45
	global_load_lds_dwordx4 v[186:187], off
	s_mov_b32 m0, s70
	v_lshl_add_u64 v[186:187], s[40:41], 0, v[162:163]
	s_add_i32 s71, s70, 0x2000
	global_load_lds_dwordx4 v[186:187], off
	v_lshl_add_u64 v[186:187], s[40:41], 0, v[164:165]
	s_mov_b32 m0, s71
	s_nop 0
	global_load_lds_dwordx4 v[186:187], off
	s_mov_b32 m0, s65
	v_lshl_add_u64 v[186:187], s[38:39], 0, v[162:163]
	global_load_lds_dwordx4 v[186:187], off
	v_lshl_add_u64 v[186:187], s[38:39], 0, v[164:165]
	s_mov_b32 m0, s66
	s_nop 0
	global_load_lds_dwordx4 v[186:187], off
	s_waitcnt vmcnt(8)
	s_waitcnt lgkmcnt(0)
	s_barrier
	s_setprio 1
	s_waitcnt lgkmcnt(0)
	v_mfma_f32_16x16x128_f8f6f4 v[86:89], v[26:33], v[178:185], v[86:89]
	v_mfma_f32_16x16x128_f8f6f4 v[82:85], v[18:25], v[178:185], v[82:85]
	v_mfma_f32_16x16x128_f8f6f4 v[70:73], v[26:33], v[194:201], v[70:73]
	v_mfma_f32_16x16x128_f8f6f4 v[66:69], v[18:25], v[194:201], v[66:69]
	v_mfma_f32_16x16x128_f8f6f4 v[58:61], v[26:33], v[214:221], v[58:61]
	v_mfma_f32_16x16x128_f8f6f4 v[50:53], v[18:25], v[214:221], v[50:53]
	v_mfma_f32_16x16x128_f8f6f4 v[46:49], v[26:33], v[222:229], v[46:49]
	v_mfma_f32_16x16x128_f8f6f4 v[38:41], v[18:25], v[222:229], v[38:41]
	s_setprio 0
	s_setprio 1
	v_mfma_f32_16x16x128_f8f6f4 v[94:97], v[10:17], v[178:185], v[94:97]
	v_mfma_f32_16x16x128_f8f6f4 v[90:93], v[2:9], v[178:185], v[90:93]
	v_mfma_f32_16x16x128_f8f6f4 v[78:81], v[10:17], v[194:201], v[78:81]
	v_mfma_f32_16x16x128_f8f6f4 v[74:77], v[2:9], v[194:201], v[74:77]
	v_mfma_f32_16x16x128_f8f6f4 v[62:65], v[10:17], v[214:221], v[62:65]
	v_mfma_f32_16x16x128_f8f6f4 v[54:57], v[2:9], v[214:221], v[54:57]
	v_mfma_f32_16x16x128_f8f6f4 v[42:45], v[10:17], v[222:229], v[42:45]
	v_mfma_f32_16x16x128_f8f6f4 v[34:37], v[2:9], v[222:229], v[34:37]
	s_setprio 0
	s_barrier
	s_mov_b32 s72, 0
	.p2align 6

; #define WAIT_BAR(N) asm volatile("s_waitcnt vmcnt(" #N ") lgkmcnt(0)\n\ts_barrier":::"memory")
;   #define DMA_K(t,slot) glds16(ksrc+(long)TILE(t)*(KVBLK*KVPT),(unsigned)__builtin_amdgcn_readfirstlane(kdst+(slot)))
;   #define DMA_V(t,slot) glds16(vsrc+(long)TILE(t)*(KVBLK*KVPT),(unsigned)__builtin_amdgcn_readfirstlane(vdst+(slot)))
;   #define CMASK(P0,P1,t) do{int jb_=(t)-(NT-nband); if(jb_>=0)wmask(P0,P1,krel0+64*jb_,qrel,hi,wq);}while(0)
;   #define START(P0,P1) do{ const float rm=rowmax(P0,P1); resc=false; \
;     { const float dl=rm; mhat=fadd_s(mhat,dl); \
;       _Pragma("unroll") for(int r=0;r<16;++r){P0[r]=fsub_s(P0[r],dl);P1[r]=fsub_s(P1[r],dl);} \
;       _Pragma("unroll") for(int r=0;r<16;++r)negm[r]=-mhat; asm volatile("":"+v"(negm)); } \
;     _Pragma("unroll") for(int r=0;r<16;++r)P0[r]=__builtin_amdgcn_exp2f(P0[r]); }while(0)
;   #define ROT() do{sl_prev=sl_cur;sl_cur=sl_next;sl_next=(sl_next==(NSLOT-1)*SLOTB)?0:sl_next+SLOTB;}while(0)
;   #define CMASK(P0,P1,t) do{}while(0)
;   #define CMASK(P0,P1,t) do{int jb_=(t)-(NT-nband); if(jb_>=0)wmask(P0,P1,krel0+64*jb_,qrel,hi,wq);}while(0)
; template<int THRL> __device__ __forceinline__ void attn_unit(const AttU&U,const bf16*Q,const bf16*__restrict__ K,const bf16*__restrict__ V,bf16*O,char*shm){
;     ...
;   f32x16 pA0,pA1,pB0,pB1;
;   int sl_prev=0,sl_cur=0,sl_next=SLOTB;
;     ...
;   DMA_K(2,2*SLOTB);
;   WAIT_BAR(3);
;   qkt(pA0,pA1,Kbase,qr,negm,r32,hi);asm volatile("s_nop 15\n\ts_nop 7":"+v"(pA0),"+v"(pA1));CMASK(pA0,pA1,0);
;   START(pA0,pA1);
;   _Pragma("unroll") for(int r=0;r<16;++r)pA1[r]=__builtin_amdgcn_exp2f(pA1[r]);
;   WAIT_BAR(0);
;   DMA_K(3,0);DMA_V(1,SLOTB);
;   ROT();
;   kload8(kf,kp0+sl_cur);
;   WAIT_BAR(2);
;     ...
;   int t=1;
;     ...
;   const int tend=__builtin_amdgcn_readfirstlane((NT-5)<(NT-nband-1)?(NT-5):(NT-nband-1));
;   for(;t<tend;t+=2){
.LBB0_914:
	v_lshlrev_b32_e32 v203, 3, v35
	v_lshlrev_b32_e32 v35, 1, v34
	v_and_b32_e32 v204, 32, v35
	v_lshlrev_b32_e32 v200, 8, v206
	v_lshlrev_b32_e32 v34, 4, v34
	s_movk_i32 s3, 0xc0
	v_and_or_b32 v202, v34, s3, v200
	v_add_u32_e32 v34, 0, v204
	v_add3_u32 v215, v34, v203, v202
	v_max3_f32 v34, v18, v19, v2
	v_max3_f32 v35, v20, v21, v3
	s_and_b32 s2, s6, 0x3fffffc0
	v_max3_f32 v34, v34, v4, v5
	v_max3_f32 v35, v35, v24, v25
	s_lshl_b32 s2, s2, 2
	v_max3_f32 v34, v34, v22, v23
	v_max3_f32 v35, v35, v8, v9
	s_add_i32 s6, s2, 0
	v_max3_f32 v34, v34, v6, v7
	v_max3_f32 v35, v35, v28, v29
	s_mov_b64 s[2:3], 0x18000
	v_max3_f32 v34, v34, v26, v27
	v_max3_f32 v35, v35, v12, v13
	s_sub_i32 s33, s5, s28
	v_max3_f32 v34, v34, v10, v11
	v_max3_f32 v35, v35, v32, v33
	s_mov_b32 s9, 1
	v_max3_f32 v34, v34, v30, v31
	v_max3_f32 v35, v35, v16, v17
	s_mov_b32 s5, 0
	v_max3_f32 v34, v34, v14, v15
	s_movk_i32 s34, 0x2000
	v_max_f32_e32 v34, v34, v35
	v_cmp_gt_u32_e64 s[36:37], 32, v199
	v_mov_b32_e32 v35, v34
	s_nop 1
	v_permlane32_swap_b32_e32 v34, v35
	v_max_f32_e32 v34, v34, v35
	v_lshl_add_u32 v205, v198, 2, s6
	v_add_f32_e32 v201, v191, v34
	v_sub_f32_e32 v18, v18, v34
	v_sub_f32_e32 v2, v2, v34
	v_sub_f32_e32 v19, v19, v34
	v_sub_f32_e32 v3, v3, v34
	v_sub_f32_e32 v20, v20, v34
	v_sub_f32_e32 v4, v4, v34
	v_sub_f32_e32 v21, v21, v34
	v_sub_f32_e32 v5, v5, v34
	v_sub_f32_e32 v22, v22, v34
	v_sub_f32_e32 v6, v6, v34
	v_sub_f32_e32 v23, v23, v34
	v_sub_f32_e32 v7, v7, v34
	v_sub_f32_e32 v24, v24, v34
	v_sub_f32_e32 v8, v8, v34
	v_sub_f32_e32 v25, v25, v34
	v_sub_f32_e32 v9, v9, v34
	v_sub_f32_e32 v26, v26, v34
	v_sub_f32_e32 v10, v10, v34
	v_sub_f32_e32 v27, v27, v34
	v_sub_f32_e32 v11, v11, v34
	v_sub_f32_e32 v28, v28, v34
	v_sub_f32_e32 v12, v12, v34
	v_sub_f32_e32 v29, v29, v34
	v_sub_f32_e32 v13, v13, v34
	v_sub_f32_e32 v30, v30, v34
	v_sub_f32_e32 v14, v14, v34
	v_sub_f32_e32 v31, v31, v34
	v_sub_f32_e32 v15, v15, v34
	v_sub_f32_e32 v32, v32, v34
	v_sub_f32_e32 v16, v16, v34
	v_sub_f32_e32 v33, v33, v34
	v_sub_f32_e32 v17, v17, v34
	s_nop 0
	v_xor_b32_e32 v34, 0x80000000, v201
	v_mov_b32_e32 v35, v34
	v_mov_b32_e32 v36, v34
	v_mov_b32_e32 v37, v34
	v_mov_b32_e32 v38, v34
	v_mov_b32_e32 v39, v34
	v_mov_b32_e32 v40, v34
	v_mov_b32_e32 v41, v34
	v_mov_b32_e32 v42, v34
	v_mov_b32_e32 v43, v34
	v_mov_b32_e32 v44, v34
	v_mov_b32_e32 v45, v34
	v_mov_b32_e32 v46, v34
	v_mov_b32_e32 v47, v34
	v_mov_b32_e32 v48, v34
	v_mov_b32_e32 v49, v34
	s_waitcnt vmcnt(0) lgkmcnt(0)
	s_barrier
	v_exp_f32_e32 v50, v2
	v_exp_f32_e32 v51, v3
	v_lshl_add_u64 v[2:3], v[82:83], 0, s[2:3]
	s_mov_b32 s2, m0
	s_mov_b32 m0, s30
	s_nop 0
	global_load_lds_dwordx4 v[2:3], off
	s_mov_b32 m0, s2
	v_lshl_add_u64 v[2:3], v[196:197], 0, s[0:1]
	s_add_i32 s0, s31, 0x2000
	s_mov_b32 s1, m0
	s_mov_b32 m0, s0
	s_nop 0
	global_load_lds_dwordx4 v[2:3], off
	s_mov_b32 m0, s1
	ds_read_b128 v[174:177], v214 offset:8192
	ds_read_b128 v[170:173], v214 offset:8704
	ds_read_b128 v[166:169], v214 offset:10240
	ds_read_b128 v[162:165], v214 offset:10752
	ds_read_b128 v[158:161], v214 offset:12288
	ds_read_b128 v[154:157], v214 offset:12800
	ds_read_b128 v[150:153], v214 offset:14336
	ds_read_b128 v[146:149], v214 offset:14848
	v_exp_f32_e32 v66, v18
	v_exp_f32_e32 v67, v19
	v_exp_f32_e32 v68, v20
	v_exp_f32_e32 v69, v21
	v_exp_f32_e32 v70, v22
	v_exp_f32_e32 v71, v23
	v_exp_f32_e32 v72, v24
	v_exp_f32_e32 v73, v25
	v_exp_f32_e32 v74, v26
	v_exp_f32_e32 v75, v27
	v_exp_f32_e32 v76, v28
	v_exp_f32_e32 v77, v29
	v_exp_f32_e32 v78, v30
	v_exp_f32_e32 v79, v31
	v_exp_f32_e32 v80, v32
	v_exp_f32_e32 v81, v33
	v_exp_f32_e32 v52, v4
	v_exp_f32_e32 v53, v5
	v_exp_f32_e32 v54, v6
	v_exp_f32_e32 v55, v7
	v_exp_f32_e32 v56, v8
	v_exp_f32_e32 v57, v9
	v_exp_f32_e32 v58, v10
	v_exp_f32_e32 v59, v11
	v_exp_f32_e32 v60, v12
	v_exp_f32_e32 v61, v13
	v_exp_f32_e32 v62, v14
	v_exp_f32_e32 v63, v15
	v_exp_f32_e32 v64, v16
	v_exp_f32_e32 v65, v17
	s_waitcnt vmcnt(2) lgkmcnt(0)
	s_barrier
	s_add_i32 s0, s22, -5
	s_add_i32 s1, s25, -1
	s_min_i32 s7, s0, s1
	s_cmp_lt_i32 s7, 2
	s_cbranch_scc1 .LBB0_930
	v_lshlrev_b32_e32 v2, 4, v206
	v_mov_b32_e32 v18, v191
	v_mov_b32_e32 v19, v191
	v_mov_b32_e32 v20, v191
	v_mov_b32_e32 v21, v191
	v_mov_b32_e32 v22, v191
	v_mov_b32_e32 v23, v191
	v_mov_b32_e32 v24, v191
	v_mov_b32_e32 v25, v191
	v_mov_b32_e32 v26, v191
	v_mov_b32_e32 v27, v191
	v_mov_b32_e32 v28, v191
	v_mov_b32_e32 v29, v191
	v_mov_b32_e32 v30, v191
	v_mov_b32_e32 v31, v191
	v_mov_b32_e32 v32, v191
	v_mov_b32_e32 v33, v191
	v_add_u32_e32 v182, s6, v2
	v_mov_b64_e32 v[2:3], v[18:19]
	s_mov_b32 s0, 0
	s_movk_i32 s5, 0x4000
	s_movk_i32 s9, 0x2000
	v_mov_b32_e32 v217, 0
	s_mov_b32 s8, 5
	v_mov_b64_e32 v[4:5], v[20:21]
	v_mov_b64_e32 v[6:7], v[22:23]
	v_mov_b64_e32 v[8:9], v[24:25]
	v_mov_b64_e32 v[10:11], v[26:27]
	v_mov_b64_e32 v[12:13], v[28:29]
	v_mov_b64_e32 v[14:15], v[30:31]
	v_mov_b64_e32 v[16:17], v[32:33]
	.p2align 6

.LBB0_1063:
	s_ashr_i32 s7, s6, 31
	s_lshl_b64 s[8:9], s[6:7], 19
	s_add_u32 s8, s96, s8
	s_addc_u32 s9, s97, s9
	s_ashr_i32 s5, s4, 31
	s_lshl_b64 s[10:11], s[4:5], 19
	s_add_u32 s10, s25, s10
	s_addc_u32 s11, s33, s11
	s_add_u32 s18, s34, 0x100
	s_addc_u32 s19, s35, 0
	s_add_u32 s40, s34, 0x180
	s_addc_u32 s41, s35, 0
	s_add_u32 s42, s30, 0x100
	s_addc_u32 s43, s31, 0
	s_add_i32 s56, 0, 0x10000
	s_add_i32 s58, 0, 0x14000
	v_add_u32_e32 v98, s56, v193
	v_add_u32_e32 v99, s58, v193
	ds_read_b128 v[2:5], v98
	ds_read_b128 v[6:9], v98 offset:1024
	ds_read_b128 v[10:13], v98 offset:2048
	ds_read_b128 v[14:17], v98 offset:3072
	ds_read_b128 v[18:21], v99
	ds_read_b128 v[22:25], v99 offset:1024
	ds_read_b128 v[26:29], v99 offset:2048
	ds_read_b128 v[30:33], v99 offset:3072
	s_mov_b64 s[38:39], 0x100
	s_add_u32 s44, s34, 0x40080
	s_addc_u32 s45, s35, 0
	s_add_i32 s5, s23, 0xc000
	ds_read_b128 v[34:37], v199
	ds_read_b128 v[38:41], v199 offset:1024
	ds_read_b128 v[42:45], v199 offset:2048
	ds_read_b128 v[46:49], v199 offset:3072
	ds_read_b128 v[50:53], v199 offset:4096
	ds_read_b128 v[54:57], v199 offset:5120
	ds_read_b128 v[58:61], v199 offset:6144
	ds_read_b128 v[62:65], v199 offset:7168
	s_mov_b32 m0, s5
	v_lshl_add_u64 v[66:67], s[44:45], 0, v[190:191]
	s_add_i32 s7, s23, 0xe000
	global_load_lds_dwordx4 v[66:67], off
	v_lshl_add_u64 v[66:67], s[44:45], 0, v[182:183]
	s_mov_b32 m0, s7
	s_nop 0
	global_load_lds_dwordx4 v[66:67], off
	s_waitcnt vmcnt(8)
	s_waitcnt lgkmcnt(0)
	s_barrier
	s_setprio 1
	s_waitcnt lgkmcnt(0)
	v_mfma_f32_16x16x32_bf16 v[66:69], v[2:5], v[34:37], 0
	v_mfma_f32_16x16x32_bf16 v[70:73], v[10:13], v[34:37], 0
	v_mfma_f32_16x16x32_bf16 v[74:77], v[2:5], v[42:45], 0
	v_mfma_f32_16x16x32_bf16 v[78:81], v[10:13], v[42:45], 0
	v_mfma_f32_16x16x32_bf16 v[82:85], v[2:5], v[50:53], 0
	v_mfma_f32_16x16x32_bf16 v[86:89], v[10:13], v[50:53], 0
	v_mfma_f32_16x16x32_bf16 v[90:93], v[2:5], v[58:61], 0
	v_mfma_f32_16x16x32_bf16 v[66:69], v[6:9], v[38:41], v[66:69]
	v_mfma_f32_16x16x32_bf16 v[70:73], v[14:17], v[38:41], v[70:73]
	v_mfma_f32_16x16x32_bf16 v[74:77], v[6:9], v[46:49], v[74:77]
	v_mfma_f32_16x16x32_bf16 v[78:81], v[14:17], v[46:49], v[78:81]
	v_mfma_f32_16x16x32_bf16 v[82:85], v[6:9], v[54:57], v[82:85]
	v_mfma_f32_16x16x32_bf16 v[86:89], v[14:17], v[54:57], v[86:89]
	v_mfma_f32_16x16x32_bf16 v[102:105], v[6:9], v[62:65], v[90:93]
	v_mfma_f32_16x16x32_bf16 v[90:93], v[10:13], v[58:61], 0
	v_mfma_f32_16x16x32_bf16 v[106:109], v[14:17], v[62:65], v[90:93]
	s_setprio 0
	s_setprio 1
	v_mfma_f32_16x16x32_bf16 v[90:93], v[18:21], v[34:37], 0
	v_mfma_f32_16x16x32_bf16 v[34:37], v[26:29], v[34:37], 0
	v_mfma_f32_16x16x32_bf16 v[110:113], v[22:25], v[38:41], v[90:93]
	v_mfma_f32_16x16x32_bf16 v[34:37], v[30:33], v[38:41], v[34:37]
	v_mfma_f32_16x16x32_bf16 v[38:41], v[18:21], v[42:45], 0
	v_mfma_f32_16x16x32_bf16 v[42:45], v[26:29], v[42:45], 0
	v_mfma_f32_16x16x32_bf16 v[38:41], v[22:25], v[46:49], v[38:41]
	v_mfma_f32_16x16x32_bf16 v[42:45], v[30:33], v[46:49], v[42:45]
	v_mfma_f32_16x16x32_bf16 v[46:49], v[18:21], v[50:53], 0
	v_mfma_f32_16x16x32_bf16 v[50:53], v[26:29], v[50:53], 0
	v_mfma_f32_16x16x32_bf16 v[46:49], v[22:25], v[54:57], v[46:49]
	v_mfma_f32_16x16x32_bf16 v[50:53], v[30:33], v[54:57], v[50:53]
	v_mfma_f32_16x16x32_bf16 v[54:57], v[18:21], v[58:61], 0
	v_mfma_f32_16x16x32_bf16 v[58:61], v[26:29], v[58:61], 0
	v_mfma_f32_16x16x32_bf16 v[54:57], v[22:25], v[62:65], v[54:57]
	v_mfma_f32_16x16x32_bf16 v[58:61], v[30:33], v[62:65], v[58:61]
	s_setprio 0
	s_barrier
	s_add_i32 s56, s56, s48
	ds_read_b128 v[62:65], v199 offset:16384
	ds_read_b128 v[90:93], v199 offset:17408
	ds_read_b128 v[94:97], v199 offset:18432
	ds_read_b128 v[114:117], v199 offset:19456
	ds_read_b128 v[118:121], v199 offset:20480
	ds_read_b128 v[122:125], v199 offset:21504
	ds_read_b128 v[126:129], v199 offset:22528
	ds_read_b128 v[130:133], v199 offset:23552
	s_mov_b32 m0, s56
	v_lshl_add_u64 v[100:101], s[42:43], 0, v[190:191]
	s_add_i32 s57, s56, 0x2000
	global_load_lds_dwordx4 v[100:101], off
	v_lshl_add_u64 v[100:101], s[42:43], 0, v[182:183]
	s_add_u32 s42, s30, 0x40100
	s_mov_b32 m0, s57
	s_addc_u32 s43, s31, 0
	s_add_i32 s58, s58, s48
	global_load_lds_dwordx4 v[100:101], off
	s_mov_b32 m0, s58
	v_lshl_add_u64 v[100:101], s[42:43], 0, v[190:191]
	s_add_i32 s59, s58, 0x2000
	global_load_lds_dwordx4 v[100:101], off
	v_lshl_add_u64 v[100:101], s[42:43], 0, v[182:183]
	s_mov_b32 m0, s59
	s_nop 0
	global_load_lds_dwordx4 v[100:101], off
	s_mov_b32 m0, s23
	v_lshl_add_u64 v[100:101], s[18:19], 0, v[190:191]
	global_load_lds_dwordx4 v[100:101], off
	v_lshl_add_u64 v[100:101], s[18:19], 0, v[182:183]
	s_mov_b32 m0, s29
	s_nop 0
	global_load_lds_dwordx4 v[100:101], off
	s_waitcnt vmcnt(8)
	s_waitcnt lgkmcnt(0)
	s_barrier
	s_setprio 1
	s_waitcnt lgkmcnt(0)
	v_mfma_f32_16x16x32_bf16 v[134:137], v[2:5], v[62:65], 0
	v_mfma_f32_16x16x32_bf16 v[146:149], v[6:9], v[90:93], v[134:137]
	v_mfma_f32_16x16x32_bf16 v[134:137], v[10:13], v[62:65], 0
	v_mfma_f32_16x16x32_bf16 v[150:153], v[14:17], v[90:93], v[134:137]
	v_mfma_f32_16x16x32_bf16 v[134:137], v[2:5], v[94:97], 0
	v_mfma_f32_16x16x32_bf16 v[154:157], v[6:9], v[114:117], v[134:137]
	v_mfma_f32_16x16x32_bf16 v[134:137], v[10:13], v[94:97], 0
	v_mfma_f32_16x16x32_bf16 v[158:161], v[14:17], v[114:117], v[134:137]
	v_mfma_f32_16x16x32_bf16 v[134:137], v[2:5], v[118:121], 0
	v_mfma_f32_16x16x32_bf16 v[2:5], v[2:5], v[126:129], 0
	v_mfma_f32_16x16x32_bf16 v[162:165], v[6:9], v[122:125], v[134:137]
	v_mfma_f32_16x16x32_bf16 v[2:5], v[6:9], v[130:133], v[2:5]
	v_mfma_f32_16x16x32_bf16 v[6:9], v[10:13], v[126:129], 0
	v_mfma_f32_16x16x32_bf16 v[134:137], v[10:13], v[118:121], 0
	v_mfma_f32_16x16x32_bf16 v[6:9], v[14:17], v[130:133], v[6:9]
	v_mfma_f32_16x16x32_bf16 v[166:169], v[14:17], v[122:125], v[134:137]
	s_setprio 0
	s_setprio 1
	v_mfma_f32_16x16x32_bf16 v[10:13], v[18:21], v[62:65], 0
	v_mfma_f32_16x16x32_bf16 v[170:173], v[22:25], v[90:93], v[10:13]
	v_mfma_f32_16x16x32_bf16 v[10:13], v[26:29], v[62:65], 0
	v_mfma_f32_16x16x32_bf16 v[174:177], v[30:33], v[90:93], v[10:13]
	v_mfma_f32_16x16x32_bf16 v[10:13], v[18:21], v[94:97], 0
	v_mfma_f32_16x16x32_bf16 v[178:181], v[22:25], v[114:117], v[10:13]
	v_mfma_f32_16x16x32_bf16 v[10:13], v[26:29], v[94:97], 0
	v_mfma_f32_16x16x32_bf16 v[184:187], v[30:33], v[114:117], v[10:13]
	v_mfma_f32_16x16x32_bf16 v[10:13], v[18:21], v[118:121], 0
	v_mfma_f32_16x16x32_bf16 v[194:197], v[22:25], v[122:125], v[10:13]
	v_mfma_f32_16x16x32_bf16 v[10:13], v[26:29], v[118:121], 0
	v_mfma_f32_16x16x32_bf16 v[118:121], v[30:33], v[122:125], v[10:13]
	v_mfma_f32_16x16x32_bf16 v[10:13], v[18:21], v[126:129], 0
	v_mfma_f32_16x16x32_bf16 v[200:203], v[22:25], v[130:133], v[10:13]
	v_mfma_f32_16x16x32_bf16 v[10:13], v[26:29], v[126:129], 0
	v_mfma_f32_16x16x32_bf16 v[204:207], v[30:33], v[130:133], v[10:13]
	s_setprio 0
	s_barrier
	s_add_i32 s61, 0, 0x18000
	s_add_i32 s63, 0, 0x1c000
	v_add_u32_e32 v100, s61, v193
	v_add_u32_e32 v101, s63, v193
	s_nop 0
	ds_read_b128 v[10:13], v100
	ds_read_b128 v[14:17], v100 offset:1024
	ds_read_b128 v[18:21], v100 offset:2048
	ds_read_b128 v[22:25], v100 offset:3072
	ds_read_b128 v[214:217], v101
	ds_read_b128 v[218:221], v101 offset:1024
	ds_read_b128 v[222:225], v101 offset:2048
	ds_read_b128 v[226:229], v101 offset:3072
	s_add_u32 s18, s34, 0x40100
	s_addc_u32 s19, s35, 0
	s_mov_b32 m0, s51
	ds_read_b128 v[26:29], v199 offset:32768
	ds_read_b128 v[30:33], v199 offset:33792
	ds_read_b128 v[62:65], v199 offset:34816
	ds_read_b128 v[230:233], v199 offset:35840
	ds_read_b128 v[234:237], v199 offset:36864
	ds_read_b128 v[238:241], v199 offset:37888
	ds_read_b128 v[242:245], v199 offset:38912
	ds_read_b128 v[246:249], v199 offset:39936
	s_nop 0
	v_lshl_add_u64 v[90:91], s[18:19], 0, v[190:191]
	global_load_lds_dwordx4 v[90:91], off
	v_lshl_add_u64 v[90:91], s[18:19], 0, v[182:183]
	s_mov_b32 m0, s52
	s_nop 0
	global_load_lds_dwordx4 v[90:91], off
	s_waitcnt vmcnt(8)
	s_waitcnt lgkmcnt(0)
	s_barrier
	s_setprio 1
	s_waitcnt lgkmcnt(0)
	v_mfma_f32_16x16x32_bf16 v[66:69], v[10:13], v[26:29], v[66:69]
	v_mfma_f32_16x16x32_bf16 v[134:137], v[14:17], v[30:33], v[66:69]
	v_mfma_f32_16x16x32_bf16 v[66:69], v[18:21], v[26:29], v[70:73]
	v_mfma_f32_16x16x32_bf16 v[142:145], v[22:25], v[30:33], v[66:69]
	v_mfma_f32_16x16x32_bf16 v[66:69], v[10:13], v[62:65], v[74:77]
	v_mfma_f32_16x16x32_bf16 v[126:129], v[14:17], v[230:233], v[66:69]
	v_mfma_f32_16x16x32_bf16 v[66:69], v[18:21], v[62:65], v[78:81]
	v_mfma_f32_16x16x32_bf16 v[122:125], v[22:25], v[230:233], v[66:69]
	v_mfma_f32_16x16x32_bf16 v[66:69], v[10:13], v[234:237], v[82:85]
	v_mfma_f32_16x16x32_bf16 v[94:97], v[14:17], v[238:241], v[66:69]
	v_mfma_f32_16x16x32_bf16 v[66:69], v[18:21], v[234:237], v[86:89]
	v_mfma_f32_16x16x32_bf16 v[90:93], v[22:25], v[238:241], v[66:69]
	v_mfma_f32_16x16x32_bf16 v[66:69], v[10:13], v[242:245], v[102:105]
	v_mfma_f32_16x16x32_bf16 v[78:81], v[14:17], v[246:249], v[66:69]
	v_mfma_f32_16x16x32_bf16 v[66:69], v[18:21], v[242:245], v[106:109]
	v_mfma_f32_16x16x32_bf16 v[70:73], v[22:25], v[246:249], v[66:69]
	s_setprio 0
	s_setprio 1
	v_mfma_f32_16x16x32_bf16 v[66:69], v[214:217], v[26:29], v[110:113]
	v_mfma_f32_16x16x32_bf16 v[26:29], v[222:225], v[26:29], v[34:37]
	v_mfma_f32_16x16x32_bf16 v[130:133], v[226:229], v[30:33], v[26:29]
	v_mfma_f32_16x16x32_bf16 v[26:29], v[214:217], v[62:65], v[38:41]
	v_mfma_f32_16x16x32_bf16 v[114:117], v[218:221], v[230:233], v[26:29]
	v_mfma_f32_16x16x32_bf16 v[26:29], v[222:225], v[62:65], v[42:45]
	v_mfma_f32_16x16x32_bf16 v[110:113], v[226:229], v[230:233], v[26:29]
	v_mfma_f32_16x16x32_bf16 v[26:29], v[214:217], v[234:237], v[46:49]
	v_mfma_f32_16x16x32_bf16 v[86:89], v[218:221], v[238:241], v[26:29]
	v_mfma_f32_16x16x32_bf16 v[26:29], v[222:225], v[234:237], v[50:53]
	v_mfma_f32_16x16x32_bf16 v[82:85], v[226:229], v[238:241], v[26:29]
	v_mfma_f32_16x16x32_bf16 v[26:29], v[214:217], v[242:245], v[54:57]
	v_mfma_f32_16x16x32_bf16 v[62:65], v[218:221], v[246:249], v[26:29]
	v_mfma_f32_16x16x32_bf16 v[26:29], v[222:225], v[242:245], v[58:61]
	v_mfma_f32_16x16x32_bf16 v[138:141], v[218:221], v[30:33], v[66:69]
	v_mfma_f32_16x16x32_bf16 v[54:57], v[226:229], v[246:249], v[26:29]
	s_setprio 0
	s_barrier
;     ...
;         PG8_TRIP(0, true);
; #pragma unroll 1
;         for (int t = 2; t < nt; t += 2) PG8_TRIP(t, false);
	s_add_u32 s18, s30, 0x180
	s_addc_u32 s19, s31, 0
	s_add_i32 s61, s61, s48
	ds_read_b128 v[34:37], v199 offset:49152
	ds_read_b128 v[38:41], v199 offset:50176
	ds_read_b128 v[102:105], v199 offset:51200
	ds_read_b128 v[106:109], v199 offset:52224
	ds_read_b128 v[230:233], v199 offset:53248
	ds_read_b128 v[234:237], v199 offset:54272
	ds_read_b128 v[238:241], v199 offset:55296
	ds_read_b128 v[242:245], v199 offset:56320
	s_mov_b32 m0, s61
	v_lshl_add_u64 v[26:27], s[18:19], 0, v[190:191]
	s_add_i32 s62, s61, 0x2000
	global_load_lds_dwordx4 v[26:27], off
	v_lshl_add_u64 v[26:27], s[18:19], 0, v[182:183]
	s_add_u32 s18, s30, 0x40180
	s_mov_b32 m0, s62
	s_addc_u32 s19, s31, 0
	s_add_i32 s63, s63, s48
	global_load_lds_dwordx4 v[26:27], off
	s_mov_b32 m0, s63
	v_lshl_add_u64 v[26:27], s[18:19], 0, v[190:191]
	s_add_i32 s64, s63, 0x2000
	global_load_lds_dwordx4 v[26:27], off
	v_lshl_add_u64 v[26:27], s[18:19], 0, v[182:183]
	s_mov_b32 m0, s64
	s_nop 0
	global_load_lds_dwordx4 v[26:27], off
	s_mov_b32 m0, s53
	v_lshl_add_u64 v[26:27], s[40:41], 0, v[190:191]
	global_load_lds_dwordx4 v[26:27], off
	v_lshl_add_u64 v[26:27], s[40:41], 0, v[182:183]
	s_mov_b32 m0, s54
	s_nop 0
	global_load_lds_dwordx4 v[26:27], off
	s_waitcnt vmcnt(8)
	s_waitcnt lgkmcnt(0)
	s_barrier
	s_setprio 1
	s_waitcnt lgkmcnt(0)
	v_mfma_f32_16x16x32_bf16 v[26:29], v[10:13], v[34:37], v[146:149]
	v_mfma_f32_16x16x32_bf16 v[74:77], v[14:17], v[38:41], v[26:29]
	v_mfma_f32_16x16x32_bf16 v[26:29], v[18:21], v[34:37], v[150:153]
	v_mfma_f32_16x16x32_bf16 v[66:69], v[22:25], v[38:41], v[26:29]
	v_mfma_f32_16x16x32_bf16 v[26:29], v[10:13], v[102:105], v[154:157]
	v_mfma_f32_16x16x32_bf16 v[46:49], v[14:17], v[106:109], v[26:29]
	v_mfma_f32_16x16x32_bf16 v[26:29], v[18:21], v[102:105], v[158:161]
	v_mfma_f32_16x16x32_bf16 v[42:45], v[22:25], v[106:109], v[26:29]
	v_mfma_f32_16x16x32_bf16 v[26:29], v[10:13], v[230:233], v[162:165]
	v_mfma_f32_16x16x32_bf16 v[2:5], v[10:13], v[238:241], v[2:5]
	v_mfma_f32_16x16x32_bf16 v[30:33], v[14:17], v[234:237], v[26:29]
	v_mfma_f32_16x16x32_bf16 v[26:29], v[18:21], v[230:233], v[166:169]
	v_mfma_f32_16x16x32_bf16 v[14:17], v[14:17], v[242:245], v[2:5]
	v_mfma_f32_16x16x32_bf16 v[2:5], v[18:21], v[238:241], v[6:9]
	v_mfma_f32_16x16x32_bf16 v[26:29], v[22:25], v[234:237], v[26:29]
	v_mfma_f32_16x16x32_bf16 v[10:13], v[22:25], v[242:245], v[2:5]
	s_setprio 0
	s_setprio 1
	v_mfma_f32_16x16x32_bf16 v[2:5], v[214:217], v[34:37], v[170:173]
	v_mfma_f32_16x16x32_bf16 v[58:61], v[218:221], v[38:41], v[2:5]
	v_mfma_f32_16x16x32_bf16 v[2:5], v[222:225], v[34:37], v[174:177]
	v_mfma_f32_16x16x32_bf16 v[50:53], v[226:229], v[38:41], v[2:5]
	v_mfma_f32_16x16x32_bf16 v[2:5], v[214:217], v[102:105], v[178:181]
	v_mfma_f32_16x16x32_bf16 v[38:41], v[218:221], v[106:109], v[2:5]
	v_mfma_f32_16x16x32_bf16 v[2:5], v[222:225], v[102:105], v[184:187]
	v_mfma_f32_16x16x32_bf16 v[34:37], v[226:229], v[106:109], v[2:5]
	v_mfma_f32_16x16x32_bf16 v[2:5], v[214:217], v[230:233], v[194:197]
	v_mfma_f32_16x16x32_bf16 v[22:25], v[218:221], v[234:237], v[2:5]
	v_mfma_f32_16x16x32_bf16 v[2:5], v[222:225], v[230:233], v[118:121]
	v_mfma_f32_16x16x32_bf16 v[18:21], v[226:229], v[234:237], v[2:5]
	v_mfma_f32_16x16x32_bf16 v[2:5], v[214:217], v[238:241], v[200:203]
	v_mfma_f32_16x16x32_bf16 v[6:9], v[218:221], v[242:245], v[2:5]
	v_mfma_f32_16x16x32_bf16 v[2:5], v[222:225], v[238:241], v[204:207]
	v_mfma_f32_16x16x32_bf16 v[2:5], v[226:229], v[242:245], v[2:5]
	s_setprio 0
	s_barrier
	s_mov_b32 s65, 0
	.p2align 6

.LBB0_1081:
	s_ashr_i32 s23, s22, 31
	s_lshl_b64 s[18:19], s[22:23], 18
	s_add_u32 s34, s96, s18
	s_addc_u32 s35, s97, s19
	s_ashr_i32 s11, s10, 31
	s_lshl_b64 s[18:19], s[10:11], 18
	s_add_u32 s38, s17, s18
	s_addc_u32 s39, s25, s19
	s_add_u32 s18, s28, 0x100
	s_addc_u32 s19, s29, 0
	s_add_u32 s40, s28, 0x180
	s_addc_u32 s41, s29, 0
	s_add_u32 s42, s8, 0x100
	s_addc_u32 s43, s9, 0
	s_add_i32 s23, 0, 0x10000
	s_add_i32 s59, 0, 0x14000
	v_add_u32_e32 v162, s23, v193
	v_add_u32_e32 v163, s59, v193
	ds_read_b128 v[2:5], v162
	ds_read_b128 v[6:9], v162 offset:1024
	ds_read_b128 v[10:13], v162 offset:2048
	ds_read_b128 v[14:17], v162 offset:3072
	ds_read_b128 v[18:21], v163
	ds_read_b128 v[22:25], v163 offset:1024
	ds_read_b128 v[26:29], v163 offset:2048
	ds_read_b128 v[30:33], v163 offset:3072
	s_mov_b64 s[30:31], 0x100
	s_add_u32 s44, s28, 0x20080
	s_addc_u32 s45, s29, 0
	s_add_i32 s3, s7, 0xc000
	ds_read_b128 v[34:37], v215
	ds_read_b128 v[38:41], v215 offset:1024
	ds_read_b128 v[42:45], v215 offset:2048
	ds_read_b128 v[46:49], v215 offset:3072
	ds_read_b128 v[50:53], v215 offset:4096
	ds_read_b128 v[54:57], v215 offset:5120
	ds_read_b128 v[58:61], v215 offset:6144
	ds_read_b128 v[62:65], v215 offset:7168
	s_mov_b32 m0, s3
	v_lshl_add_u64 v[66:67], s[44:45], 0, v[190:191]
	s_add_i32 s11, s7, 0xe000
	global_load_lds_dwordx4 v[66:67], off
	v_lshl_add_u64 v[66:67], s[44:45], 0, v[178:179]
	s_mov_b32 m0, s11
	s_nop 0
	global_load_lds_dwordx4 v[66:67], off
	s_waitcnt vmcnt(8)
	s_waitcnt lgkmcnt(0)
	s_barrier
	s_setprio 1
	s_waitcnt lgkmcnt(0)
	v_mfma_f32_16x16x128_f8f6f4 v[146:149], v[2:9], v[34:41], 0
	v_mfma_f32_16x16x128_f8f6f4 v[150:153], v[10:17], v[34:41], 0
	v_mfma_f32_16x16x128_f8f6f4 v[138:141], v[2:9], v[42:49], 0
	v_mfma_f32_16x16x128_f8f6f4 v[130:133], v[10:17], v[42:49], 0
	v_mfma_f32_16x16x128_f8f6f4 v[126:129], v[2:9], v[50:57], 0
	v_mfma_f32_16x16x128_f8f6f4 v[118:121], v[10:17], v[50:57], 0
	v_mfma_f32_16x16x128_f8f6f4 v[106:109], v[2:9], v[58:65], 0
	v_mfma_f32_16x16x128_f8f6f4 v[94:97], v[10:17], v[58:65], 0
	s_setprio 0
	s_setprio 1
	v_mfma_f32_16x16x128_f8f6f4 v[154:157], v[18:25], v[34:41], 0
	v_mfma_f32_16x16x128_f8f6f4 v[158:161], v[26:33], v[34:41], 0
	v_mfma_f32_16x16x128_f8f6f4 v[142:145], v[18:25], v[42:49], 0
	v_mfma_f32_16x16x128_f8f6f4 v[134:137], v[26:33], v[42:49], 0
	v_mfma_f32_16x16x128_f8f6f4 v[122:125], v[18:25], v[50:57], 0
	v_mfma_f32_16x16x128_f8f6f4 v[114:117], v[26:33], v[50:57], 0
	v_mfma_f32_16x16x128_f8f6f4 v[86:89], v[18:25], v[58:65], 0
	v_mfma_f32_16x16x128_f8f6f4 v[82:85], v[26:33], v[58:65], 0
	s_setprio 0
	s_barrier
	s_add_i32 s23, s23, s33
	ds_read_b128 v[34:37], v215 offset:16384
	ds_read_b128 v[38:41], v215 offset:17408
	ds_read_b128 v[50:53], v215 offset:18432
	ds_read_b128 v[54:57], v215 offset:19456
	ds_read_b128 v[164:167], v215 offset:20480
	ds_read_b128 v[168:171], v215 offset:21504
	ds_read_b128 v[180:183], v215 offset:22528
	ds_read_b128 v[184:187], v215 offset:23552
	s_mov_b32 m0, s23
	v_lshl_add_u64 v[42:43], s[42:43], 0, v[190:191]
	s_add_i32 s58, s23, 0x2000
	global_load_lds_dwordx4 v[42:43], off
	v_lshl_add_u64 v[42:43], s[42:43], 0, v[178:179]
	s_add_u32 s42, s8, 0x20100
	s_mov_b32 m0, s58
	s_addc_u32 s43, s9, 0
	s_add_i32 s59, s59, s33
	global_load_lds_dwordx4 v[42:43], off
	s_mov_b32 m0, s59
	v_lshl_add_u64 v[42:43], s[42:43], 0, v[190:191]
	s_add_i32 s61, s59, 0x2000
	global_load_lds_dwordx4 v[42:43], off
	v_lshl_add_u64 v[42:43], s[42:43], 0, v[178:179]
	s_mov_b32 m0, s61
	s_nop 0
	global_load_lds_dwordx4 v[42:43], off
	s_mov_b32 m0, s7
	v_lshl_add_u64 v[42:43], s[18:19], 0, v[190:191]
	global_load_lds_dwordx4 v[42:43], off
	v_lshl_add_u64 v[42:43], s[18:19], 0, v[178:179]
	s_mov_b32 m0, s52
	s_nop 0
	global_load_lds_dwordx4 v[42:43], off
	s_waitcnt vmcnt(8)
	s_waitcnt lgkmcnt(0)
	s_barrier
	s_setprio 1
	s_waitcnt lgkmcnt(0)
	v_mfma_f32_16x16x128_f8f6f4 v[110:113], v[2:9], v[34:41], 0
	v_mfma_f32_16x16x128_f8f6f4 v[98:101], v[10:17], v[34:41], 0
	v_mfma_f32_16x16x128_f8f6f4 v[78:81], v[2:9], v[50:57], 0
	v_mfma_f32_16x16x128_f8f6f4 v[74:77], v[10:17], v[50:57], 0
	v_mfma_f32_16x16x128_f8f6f4 v[62:65], v[2:9], v[164:171], 0
	v_mfma_f32_16x16x128_f8f6f4 v[58:61], v[10:17], v[164:171], 0
	v_mfma_f32_16x16x128_f8f6f4 v[46:49], v[2:9], v[180:187], 0
	v_mfma_f32_16x16x128_f8f6f4 v[42:45], v[10:17], v[180:187], 0
	s_setprio 0
	s_setprio 1
	v_mfma_f32_16x16x128_f8f6f4 v[102:105], v[18:25], v[34:41], 0
	v_mfma_f32_16x16x128_f8f6f4 v[90:93], v[26:33], v[34:41], 0
	v_mfma_f32_16x16x128_f8f6f4 v[70:73], v[18:25], v[50:57], 0
	v_mfma_f32_16x16x128_f8f6f4 v[66:69], v[26:33], v[50:57], 0
	v_mfma_f32_16x16x128_f8f6f4 v[54:57], v[18:25], v[164:171], 0
	v_mfma_f32_16x16x128_f8f6f4 v[50:53], v[26:33], v[164:171], 0
	v_mfma_f32_16x16x128_f8f6f4 v[38:41], v[18:25], v[180:187], 0
	v_mfma_f32_16x16x128_f8f6f4 v[34:37], v[26:33], v[180:187], 0
	s_setprio 0
	s_barrier
;     ...
;         PG8_TRIP(0, true);
; #pragma unroll 1
;         for (int t = 2; t < nt; t += 2) PG8_TRIP(t, false);
	s_add_i32 s44, 0, 0x18000
	s_add_i32 s62, 0, 0x1c000
	v_add_u32_e32 v164, s44, v193
	v_add_u32_e32 v165, s62, v193
	ds_read_b128 v[26:29], v164
	ds_read_b128 v[30:33], v164 offset:1024
	ds_read_b128 v[18:21], v164 offset:2048
	ds_read_b128 v[22:25], v164 offset:3072
	ds_read_b128 v[10:13], v165
	ds_read_b128 v[14:17], v165 offset:1024
	ds_read_b128 v[2:5], v165 offset:2048
	ds_read_b128 v[6:9], v165 offset:3072
	s_add_u32 s18, s28, 0x20100
	s_addc_u32 s19, s29, 0
	s_mov_b32 m0, s53
	ds_read_b128 v[166:169], v215 offset:32768
	ds_read_b128 v[170:173], v215 offset:33792
	ds_read_b128 v[180:183], v215 offset:34816
	ds_read_b128 v[184:187], v215 offset:35840
	ds_read_b128 v[194:197], v215 offset:36864
	ds_read_b128 v[198:201], v215 offset:37888
	ds_read_b128 v[216:219], v215 offset:38912
	ds_read_b128 v[220:223], v215 offset:39936
	s_nop 0
	v_lshl_add_u64 v[174:175], s[18:19], 0, v[190:191]
	global_load_lds_dwordx4 v[174:175], off
	v_lshl_add_u64 v[174:175], s[18:19], 0, v[178:179]
	s_mov_b32 m0, s54
	s_nop 0
	global_load_lds_dwordx4 v[174:175], off
	s_waitcnt vmcnt(8)
	s_waitcnt lgkmcnt(0)
	s_barrier
	s_setprio 1
	s_waitcnt lgkmcnt(0)
	v_mfma_f32_16x16x128_f8f6f4 v[146:149], v[26:33], v[166:173], v[146:149]
	v_mfma_f32_16x16x128_f8f6f4 v[150:153], v[18:25], v[166:173], v[150:153]
	v_mfma_f32_16x16x128_f8f6f4 v[138:141], v[26:33], v[180:187], v[138:141]
	v_mfma_f32_16x16x128_f8f6f4 v[130:133], v[18:25], v[180:187], v[130:133]
	v_mfma_f32_16x16x128_f8f6f4 v[126:129], v[26:33], v[194:201], v[126:129]
	v_mfma_f32_16x16x128_f8f6f4 v[118:121], v[18:25], v[194:201], v[118:121]
	v_mfma_f32_16x16x128_f8f6f4 v[106:109], v[26:33], v[216:223], v[106:109]
	v_mfma_f32_16x16x128_f8f6f4 v[94:97], v[18:25], v[216:223], v[94:97]
	s_setprio 0
	s_setprio 1
	v_mfma_f32_16x16x128_f8f6f4 v[154:157], v[10:17], v[166:173], v[154:157]
	v_mfma_f32_16x16x128_f8f6f4 v[158:161], v[2:9], v[166:173], v[158:161]
	v_mfma_f32_16x16x128_f8f6f4 v[142:145], v[10:17], v[180:187], v[142:145]
	v_mfma_f32_16x16x128_f8f6f4 v[134:137], v[2:9], v[180:187], v[134:137]
	v_mfma_f32_16x16x128_f8f6f4 v[122:125], v[10:17], v[194:201], v[122:125]
	v_mfma_f32_16x16x128_f8f6f4 v[114:117], v[2:9], v[194:201], v[114:117]
	v_mfma_f32_16x16x128_f8f6f4 v[86:89], v[10:17], v[216:223], v[86:89]
	v_mfma_f32_16x16x128_f8f6f4 v[82:85], v[2:9], v[216:223], v[82:85]
	s_setprio 0
	s_barrier
	s_add_u32 s42, s8, 0x180
	s_addc_u32 s43, s9, 0
	s_add_i32 s18, s44, s33
	ds_read_b128 v[166:169], v215 offset:49152
	ds_read_b128 v[170:173], v215 offset:50176
	ds_read_b128 v[180:183], v215 offset:51200
	ds_read_b128 v[184:187], v215 offset:52224
	ds_read_b128 v[194:197], v215 offset:53248
	ds_read_b128 v[198:201], v215 offset:54272
	ds_read_b128 v[216:219], v215 offset:55296
	ds_read_b128 v[220:223], v215 offset:56320
	s_mov_b32 m0, s18
	v_lshl_add_u64 v[174:175], s[42:43], 0, v[190:191]
	s_add_i32 s19, s18, 0x2000
	global_load_lds_dwordx4 v[174:175], off
	v_lshl_add_u64 v[174:175], s[42:43], 0, v[178:179]
	s_add_u32 s42, s8, 0x20180
	s_mov_b32 m0, s19
	s_addc_u32 s43, s9, 0
	s_add_i32 s62, s62, s33
	global_load_lds_dwordx4 v[174:175], off
	s_mov_b32 m0, s62
	v_lshl_add_u64 v[174:175], s[42:43], 0, v[190:191]
	s_add_i32 s63, s62, 0x2000
	global_load_lds_dwordx4 v[174:175], off
	v_lshl_add_u64 v[174:175], s[42:43], 0, v[178:179]
	s_mov_b32 m0, s63
	s_nop 0
	global_load_lds_dwordx4 v[174:175], off
	s_mov_b32 m0, s55
	v_lshl_add_u64 v[174:175], s[40:41], 0, v[190:191]
	global_load_lds_dwordx4 v[174:175], off
	v_lshl_add_u64 v[174:175], s[40:41], 0, v[178:179]
	s_mov_b32 m0, s56
	s_nop 0
	global_load_lds_dwordx4 v[174:175], off
	s_waitcnt vmcnt(8)
	s_waitcnt lgkmcnt(0)
	s_barrier
	s_setprio 1
	s_waitcnt lgkmcnt(0)
	v_mfma_f32_16x16x128_f8f6f4 v[110:113], v[26:33], v[166:173], v[110:113]
	v_mfma_f32_16x16x128_f8f6f4 v[98:101], v[18:25], v[166:173], v[98:101]
	v_mfma_f32_16x16x128_f8f6f4 v[78:81], v[26:33], v[180:187], v[78:81]
	v_mfma_f32_16x16x128_f8f6f4 v[74:77], v[18:25], v[180:187], v[74:77]
	v_mfma_f32_16x16x128_f8f6f4 v[62:65], v[26:33], v[194:201], v[62:65]
	v_mfma_f32_16x16x128_f8f6f4 v[58:61], v[18:25], v[194:201], v[58:61]
	v_mfma_f32_16x16x128_f8f6f4 v[46:49], v[26:33], v[216:223], v[46:49]
	v_mfma_f32_16x16x128_f8f6f4 v[42:45], v[18:25], v[216:223], v[42:45]
	s_setprio 0
	s_setprio 1
	v_mfma_f32_16x16x128_f8f6f4 v[102:105], v[10:17], v[166:173], v[102:105]
	v_mfma_f32_16x16x128_f8f6f4 v[90:93], v[2:9], v[166:173], v[90:93]
	v_mfma_f32_16x16x128_f8f6f4 v[70:73], v[10:17], v[180:187], v[70:73]
	v_mfma_f32_16x16x128_f8f6f4 v[66:69], v[2:9], v[180:187], v[66:69]
	v_mfma_f32_16x16x128_f8f6f4 v[54:57], v[10:17], v[194:201], v[54:57]
	v_mfma_f32_16x16x128_f8f6f4 v[50:53], v[2:9], v[194:201], v[50:53]
	v_mfma_f32_16x16x128_f8f6f4 v[38:41], v[10:17], v[216:223], v[38:41]
	v_mfma_f32_16x16x128_f8f6f4 v[34:37], v[2:9], v[216:223], v[34:37]
	s_setprio 0
	s_barrier
	s_mov_b32 s64, 0
	.p2align 6

.LBB0_1423:
	s_ashr_i32 s7, s6, 31
	s_lshl_b64 s[8:9], s[6:7], 18
	s_add_u32 s8, s17, s8
	s_addc_u32 s9, s25, s9
	s_add_u32 s18, s10, 0x100
	s_addc_u32 s19, s11, 0
	s_add_i32 s53, 0, 0x10000
	s_add_i32 s30, 0, 0x14000
	v_add_u32_e32 v181, s53, v176
	v_add_u32_e32 v182, s30, v176
	ds_read_b128 v[2:5], v181
	ds_read_b128 v[6:9], v181 offset:1024
	ds_read_b128 v[10:13], v181 offset:2048
	ds_read_b128 v[14:17], v181 offset:3072
	ds_read_b128 v[18:21], v182
	ds_read_b128 v[22:25], v182 offset:1024
	ds_read_b128 v[26:29], v182 offset:2048
	ds_read_b128 v[30:33], v182 offset:3072
	v_readlane_b32 s28, v254, 11
	s_add_i32 s7, s40, 0xc000
	v_readlane_b32 s29, v254, 12
	s_mov_b32 m0, s7
	s_add_i32 s52, s40, 0xe000
	ds_read_b128 v[34:37], v171
	ds_read_b128 v[38:41], v171 offset:1024
	ds_read_b128 v[42:45], v171 offset:2048
	ds_read_b128 v[46:49], v171 offset:3072
	ds_read_b128 v[50:53], v171 offset:4096
	ds_read_b128 v[54:57], v171 offset:5120
	ds_read_b128 v[58:61], v171 offset:6144
	ds_read_b128 v[62:65], v171 offset:7168
	v_mov_b32_e32 v167, v191
	global_load_lds_dwordx4 v190, s[28:29]
	s_mov_b32 m0, s52
	s_nop 0
	global_load_lds_dwordx4 v166, s[28:29]
	s_waitcnt vmcnt(8)
	s_waitcnt lgkmcnt(0)
	s_barrier
	s_setprio 1
	s_waitcnt lgkmcnt(0)
	v_mfma_f32_16x16x128_f8f6f4 v[150:153], v[2:9], v[34:41], 0
	v_mfma_f32_16x16x128_f8f6f4 v[146:149], v[10:17], v[34:41], 0
	v_mfma_f32_16x16x128_f8f6f4 v[134:137], v[2:9], v[42:49], 0
	v_mfma_f32_16x16x128_f8f6f4 v[130:133], v[10:17], v[42:49], 0
	v_mfma_f32_16x16x128_f8f6f4 v[118:121], v[2:9], v[50:57], 0
	v_mfma_f32_16x16x128_f8f6f4 v[114:117], v[10:17], v[50:57], 0
	v_mfma_f32_16x16x128_f8f6f4 v[90:93], v[2:9], v[58:65], 0
	v_mfma_f32_16x16x128_f8f6f4 v[82:85], v[10:17], v[58:65], 0
	s_setprio 0
	s_setprio 1
	v_mfma_f32_16x16x128_f8f6f4 v[158:161], v[18:25], v[34:41], 0
	v_mfma_f32_16x16x128_f8f6f4 v[154:157], v[26:33], v[34:41], 0
	v_mfma_f32_16x16x128_f8f6f4 v[142:145], v[18:25], v[42:49], 0
	v_mfma_f32_16x16x128_f8f6f4 v[138:141], v[26:33], v[42:49], 0
	v_mfma_f32_16x16x128_f8f6f4 v[126:129], v[18:25], v[50:57], 0
	v_mfma_f32_16x16x128_f8f6f4 v[122:125], v[26:33], v[50:57], 0
	v_mfma_f32_16x16x128_f8f6f4 v[102:105], v[18:25], v[58:65], 0
	v_mfma_f32_16x16x128_f8f6f4 v[98:101], v[26:33], v[58:65], 0
	s_setprio 0
	s_barrier
	s_add_i32 s53, s53, s33
	ds_read_b128 v[42:45], v171 offset:16384
	ds_read_b128 v[46:49], v171 offset:17408
	ds_read_b128 v[58:61], v171 offset:18432
	ds_read_b128 v[62:65], v171 offset:19456
	ds_read_b128 v[194:197], v171 offset:20480
	ds_read_b128 v[198:201], v171 offset:21504
	ds_read_b128 v[214:217], v171 offset:22528
	ds_read_b128 v[218:221], v171 offset:23552
	s_mov_b32 m0, s53
	v_lshl_add_u64 v[34:35], s[18:19], 0, v[164:165]
	global_load_lds_dwordx4 v[34:35], off
	v_lshl_add_u64 v[34:35], s[18:19], 0, v[162:163]
	s_add_i32 s18, s53, 0x2000
	s_add_u32 s28, s10, 0x20100
	s_mov_b32 m0, s18
	s_addc_u32 s29, s11, 0
	s_add_i32 s19, s30, s33
	global_load_lds_dwordx4 v[34:35], off
	s_mov_b32 m0, s19
	v_lshl_add_u64 v[34:35], s[28:29], 0, v[164:165]
	s_add_i32 s54, s19, 0x2000
	v_readlane_b32 s30, v254, 13
	global_load_lds_dwordx4 v[34:35], off
	v_lshl_add_u64 v[34:35], s[28:29], 0, v[162:163]
	s_mov_b32 m0, s54
	v_readlane_b32 s31, v254, 14
	global_load_lds_dwordx4 v[34:35], off
	s_mov_b64 s[28:29], s[30:31]
	s_mov_b32 m0, s40
	s_nop 0
	global_load_lds_dwordx4 v170, s[28:29]
	s_mov_b32 m0, s41
	s_nop 0
	global_load_lds_dwordx4 v168, s[28:29]
	s_waitcnt vmcnt(8)
	s_waitcnt lgkmcnt(0)
	s_barrier
	s_setprio 1
	s_waitcnt lgkmcnt(0)
	v_mfma_f32_16x16x128_f8f6f4 v[94:97], v[2:9], v[42:49], 0
	v_mfma_f32_16x16x128_f8f6f4 v[86:89], v[10:17], v[42:49], 0
	v_mfma_f32_16x16x128_f8f6f4 v[70:73], v[2:9], v[58:65], 0
	v_mfma_f32_16x16x128_f8f6f4 v[66:69], v[10:17], v[58:65], 0
	v_mfma_f32_16x16x128_f8f6f4 v[54:57], v[2:9], v[194:201], 0
	v_mfma_f32_16x16x128_f8f6f4 v[50:53], v[10:17], v[194:201], 0
	v_mfma_f32_16x16x128_f8f6f4 v[38:41], v[2:9], v[214:221], 0
	v_mfma_f32_16x16x128_f8f6f4 v[34:37], v[10:17], v[214:221], 0
	s_setprio 0
	s_setprio 1
	v_mfma_f32_16x16x128_f8f6f4 v[110:113], v[18:25], v[42:49], 0
	v_mfma_f32_16x16x128_f8f6f4 v[106:109], v[26:33], v[42:49], 0
	v_mfma_f32_16x16x128_f8f6f4 v[78:81], v[18:25], v[58:65], 0
	v_mfma_f32_16x16x128_f8f6f4 v[74:77], v[26:33], v[58:65], 0
	v_mfma_f32_16x16x128_f8f6f4 v[62:65], v[18:25], v[194:201], 0
	v_mfma_f32_16x16x128_f8f6f4 v[58:61], v[26:33], v[194:201], 0
	v_mfma_f32_16x16x128_f8f6f4 v[46:49], v[18:25], v[214:221], 0
	v_mfma_f32_16x16x128_f8f6f4 v[42:45], v[26:33], v[214:221], 0
	s_setprio 0
	s_barrier
;     ...
;         PG8_TRIP(0, true);
; #pragma unroll 1
;         for (int t = 2; t < nt; t += 2) PG8_TRIP(t, false);
	s_add_i32 s55, 0, 0x18000
	s_add_i32 s57, 0, 0x1c000
	v_add_u32_e32 v183, s55, v176
	v_add_u32_e32 v184, s57, v176
	ds_read_b128 v[26:29], v183
	ds_read_b128 v[30:33], v183 offset:1024
	ds_read_b128 v[18:21], v183 offset:2048
	ds_read_b128 v[22:25], v183 offset:3072
	ds_read_b128 v[10:13], v184
	ds_read_b128 v[14:17], v184 offset:1024
	ds_read_b128 v[2:5], v184 offset:2048
	ds_read_b128 v[6:9], v184 offset:3072
	s_mov_b64 s[28:29], s[30:31]
	s_mov_b32 m0, s42
	ds_read_b128 v[194:197], v171 offset:32768
	ds_read_b128 v[198:201], v171 offset:33792
	ds_read_b128 v[214:217], v171 offset:34816
	ds_read_b128 v[218:221], v171 offset:35840
	ds_read_b128 v[222:225], v171 offset:36864
	ds_read_b128 v[226:229], v171 offset:37888
	ds_read_b128 v[230:233], v171 offset:38912
	ds_read_b128 v[234:237], v171 offset:39936
	s_nop 0
	global_load_lds_dwordx4 v190, s[28:29]
	s_mov_b32 m0, s43
	s_nop 0
	global_load_lds_dwordx4 v166, s[28:29]
	s_waitcnt vmcnt(8)
	s_waitcnt lgkmcnt(0)
	s_barrier
	s_setprio 1
	s_waitcnt lgkmcnt(0)
	v_mfma_f32_16x16x128_f8f6f4 v[150:153], v[26:33], v[194:201], v[150:153]
	v_mfma_f32_16x16x128_f8f6f4 v[146:149], v[18:25], v[194:201], v[146:149]
	v_mfma_f32_16x16x128_f8f6f4 v[134:137], v[26:33], v[214:221], v[134:137]
	v_mfma_f32_16x16x128_f8f6f4 v[130:133], v[18:25], v[214:221], v[130:133]
	v_mfma_f32_16x16x128_f8f6f4 v[118:121], v[26:33], v[222:229], v[118:121]
	v_mfma_f32_16x16x128_f8f6f4 v[114:117], v[18:25], v[222:229], v[114:117]
	v_mfma_f32_16x16x128_f8f6f4 v[90:93], v[26:33], v[230:237], v[90:93]
	v_mfma_f32_16x16x128_f8f6f4 v[82:85], v[18:25], v[230:237], v[82:85]
	s_setprio 0
	s_setprio 1
	v_mfma_f32_16x16x128_f8f6f4 v[158:161], v[10:17], v[194:201], v[158:161]
	v_mfma_f32_16x16x128_f8f6f4 v[154:157], v[2:9], v[194:201], v[154:157]
	v_mfma_f32_16x16x128_f8f6f4 v[142:145], v[10:17], v[214:221], v[142:145]
	v_mfma_f32_16x16x128_f8f6f4 v[138:141], v[2:9], v[214:221], v[138:141]
	v_mfma_f32_16x16x128_f8f6f4 v[126:129], v[10:17], v[222:229], v[126:129]
	v_mfma_f32_16x16x128_f8f6f4 v[122:125], v[2:9], v[222:229], v[122:125]
	v_mfma_f32_16x16x128_f8f6f4 v[102:105], v[10:17], v[230:237], v[102:105]
	v_mfma_f32_16x16x128_f8f6f4 v[98:101], v[2:9], v[230:237], v[98:101]
	s_setprio 0
	s_barrier
	s_add_u32 s28, s10, 0x180
	s_addc_u32 s29, s11, 0
	s_add_i32 s55, s55, s33
	ds_read_b128 v[194:197], v171 offset:49152
	ds_read_b128 v[198:201], v171 offset:50176
	ds_read_b128 v[214:217], v171 offset:51200
	ds_read_b128 v[218:221], v171 offset:52224
	ds_read_b128 v[222:225], v171 offset:53248
	ds_read_b128 v[226:229], v171 offset:54272
	ds_read_b128 v[230:233], v171 offset:55296
	ds_read_b128 v[234:237], v171 offset:56320
	s_mov_b32 m0, s55
	v_lshl_add_u64 v[186:187], s[28:29], 0, v[164:165]
	s_add_i32 s56, s55, 0x2000
	global_load_lds_dwordx4 v[186:187], off
	v_lshl_add_u64 v[186:187], s[28:29], 0, v[162:163]
	s_add_u32 s28, s10, 0x20180
	s_mov_b32 m0, s56
	s_addc_u32 s29, s11, 0
	s_add_i32 s57, s57, s33
	global_load_lds_dwordx4 v[186:187], off
	s_mov_b32 m0, s57
	v_lshl_add_u64 v[186:187], s[28:29], 0, v[164:165]
	s_add_i32 s58, s57, 0x2000
	global_load_lds_dwordx4 v[186:187], off
	v_lshl_add_u64 v[186:187], s[28:29], 0, v[162:163]
	s_mov_b32 m0, s58
	v_readlane_b32 s28, v254, 15
	global_load_lds_dwordx4 v[186:187], off
	v_readlane_b32 s29, v254, 16
	s_mov_b32 m0, s44
	s_nop 3
	global_load_lds_dwordx4 v170, s[28:29]
	s_mov_b32 m0, s45
	s_nop 0
	global_load_lds_dwordx4 v168, s[28:29]
	s_waitcnt vmcnt(8)
	s_waitcnt lgkmcnt(0)
	s_barrier
	s_setprio 1
	s_waitcnt lgkmcnt(0)
	v_mfma_f32_16x16x128_f8f6f4 v[94:97], v[26:33], v[194:201], v[94:97]
	v_mfma_f32_16x16x128_f8f6f4 v[86:89], v[18:25], v[194:201], v[86:89]
	v_mfma_f32_16x16x128_f8f6f4 v[70:73], v[26:33], v[214:221], v[70:73]
	v_mfma_f32_16x16x128_f8f6f4 v[66:69], v[18:25], v[214:221], v[66:69]
	v_mfma_f32_16x16x128_f8f6f4 v[54:57], v[26:33], v[222:229], v[54:57]
	v_mfma_f32_16x16x128_f8f6f4 v[50:53], v[18:25], v[222:229], v[50:53]
	v_mfma_f32_16x16x128_f8f6f4 v[38:41], v[26:33], v[230:237], v[38:41]
	v_mfma_f32_16x16x128_f8f6f4 v[34:37], v[18:25], v[230:237], v[34:37]
	s_setprio 0
	s_setprio 1
	v_mfma_f32_16x16x128_f8f6f4 v[110:113], v[10:17], v[194:201], v[110:113]
	v_mfma_f32_16x16x128_f8f6f4 v[106:109], v[2:9], v[194:201], v[106:109]
	v_mfma_f32_16x16x128_f8f6f4 v[78:81], v[10:17], v[214:221], v[78:81]
	v_mfma_f32_16x16x128_f8f6f4 v[74:77], v[2:9], v[214:221], v[74:77]
	v_mfma_f32_16x16x128_f8f6f4 v[62:65], v[10:17], v[222:229], v[62:65]
	v_mfma_f32_16x16x128_f8f6f4 v[58:61], v[2:9], v[222:229], v[58:61]
	v_mfma_f32_16x16x128_f8f6f4 v[46:49], v[10:17], v[230:237], v[46:49]
	v_mfma_f32_16x16x128_f8f6f4 v[42:45], v[2:9], v[230:237], v[42:45]
	s_setprio 0
	s_barrier
	s_mov_b32 s59, 0
	s_mov_b64 s[28:29], 0x1b300100
	.p2align 6

; #define PG8_GLOAD(vo, ui_) do { if constexpr (GATHER) { _Pragma("unroll") for (int _h = 0; _h < 2; ++_h) _Pragma("unroll") for (int _i = 0; _i < 2; ++_i) (vo)[_h][_i] = gtab[(ui_) * 256 + _h * 128 + RA[_i]] + voffA[_i]; } } while (0)
;     ...
;         const bool has_next = S.next(ui + 1, nxt);
;         const char* nA = GATHER ? (const char*)A : (has_next ? (const char*)A + (size_t)nxt.pm * tstep : cA); const char* nB = has_next ? (const char*)Bt + (size_t)nxt.pn * tstep : cB;
;         if constexpr (GATHER) { if (has_next) { PG8_GLOAD(nvo, ui + 1); } }
.LBB0_1498:
	s_ashr_i32 s11, s10, 31
	s_lshl_b64 s[8:9], s[10:11], 18
	v_readlane_b32 s18, v252, 13
	v_readlane_b32 s19, v252, 14
	s_add_u32 s36, s18, s8
	s_addc_u32 s37, s19, s9
	s_ashr_i32 s35, s34, 31
	s_lshl_b64 s[8:9], s[34:35], 18
	s_add_u32 s38, s17, s8
	s_addc_u32 s39, s25, s9
	s_add_u32 s18, s6, 0x100
	s_addc_u32 s19, s7, 0
	s_add_u32 s28, s6, 0x180
	s_addc_u32 s29, s7, 0
	s_add_u32 s30, s2, 0x100
	s_addc_u32 s31, s3, 0
	s_add_i32 s55, 0, 0x10000
	s_add_i32 s57, 0, 0x14000
	v_add_u32_e32 v166, s55, v169
	v_add_u32_e32 v167, s57, v169
	ds_read_b128 v[2:5], v166
	ds_read_b128 v[6:9], v166 offset:1024
	ds_read_b128 v[10:13], v166 offset:2048
	ds_read_b128 v[14:17], v166 offset:3072
	ds_read_b128 v[18:21], v167
	ds_read_b128 v[22:25], v167 offset:1024
	ds_read_b128 v[26:29], v167 offset:2048
	ds_read_b128 v[30:33], v167 offset:3072
	s_mov_b64 s[8:9], 0x100
	s_add_u32 s40, s6, 0x20080
	s_addc_u32 s41, s7, 0
	s_add_i32 s11, s44, 0xc000
	ds_read_b128 v[34:37], v173
	ds_read_b128 v[38:41], v173 offset:1024
	ds_read_b128 v[42:45], v173 offset:2048
	ds_read_b128 v[46:49], v173 offset:3072
	ds_read_b128 v[50:53], v173 offset:4096
	ds_read_b128 v[54:57], v173 offset:5120
	ds_read_b128 v[58:61], v173 offset:6144
	ds_read_b128 v[62:65], v173 offset:7168
	s_mov_b32 m0, s11
	v_lshl_add_u64 v[66:67], s[40:41], 0, v[164:165]
	s_add_i32 s35, s44, 0xe000
	global_load_lds_dwordx4 v[66:67], off
	v_lshl_add_u64 v[66:67], s[40:41], 0, v[162:163]
	s_mov_b32 m0, s35
	s_nop 0
	global_load_lds_dwordx4 v[66:67], off
	s_waitcnt vmcnt(8)
	s_waitcnt lgkmcnt(0)
	s_barrier
	s_setprio 1
	s_waitcnt lgkmcnt(0)
	v_mfma_f32_16x16x128_f8f6f4 v[154:157], v[2:9], v[34:41], 0
	v_mfma_f32_16x16x128_f8f6f4 v[158:161], v[10:17], v[34:41], 0
	v_mfma_f32_16x16x128_f8f6f4 v[138:141], v[2:9], v[42:49], 0
	v_mfma_f32_16x16x128_f8f6f4 v[130:133], v[10:17], v[42:49], 0
	v_mfma_f32_16x16x128_f8f6f4 v[126:129], v[2:9], v[50:57], 0
	v_mfma_f32_16x16x128_f8f6f4 v[122:125], v[10:17], v[50:57], 0
	v_mfma_f32_16x16x128_f8f6f4 v[110:113], v[2:9], v[58:65], 0
	v_mfma_f32_16x16x128_f8f6f4 v[106:109], v[10:17], v[58:65], 0
	s_setprio 0
	s_setprio 1
	v_mfma_f32_16x16x128_f8f6f4 v[146:149], v[18:25], v[34:41], 0
	v_mfma_f32_16x16x128_f8f6f4 v[150:153], v[26:33], v[34:41], 0
	v_mfma_f32_16x16x128_f8f6f4 v[142:145], v[18:25], v[42:49], 0
	v_mfma_f32_16x16x128_f8f6f4 v[134:137], v[26:33], v[42:49], 0
	v_mfma_f32_16x16x128_f8f6f4 v[118:121], v[18:25], v[50:57], 0
	v_mfma_f32_16x16x128_f8f6f4 v[114:117], v[26:33], v[50:57], 0
	v_mfma_f32_16x16x128_f8f6f4 v[94:97], v[18:25], v[58:65], 0
	v_mfma_f32_16x16x128_f8f6f4 v[90:93], v[26:33], v[58:65], 0
	s_setprio 0
	s_barrier
	s_add_i32 s55, s55, s33
	ds_read_b128 v[34:37], v173 offset:16384
	ds_read_b128 v[38:41], v173 offset:17408
	ds_read_b128 v[50:53], v173 offset:18432
	ds_read_b128 v[54:57], v173 offset:19456
	ds_read_b128 v[174:177], v173 offset:20480
	ds_read_b128 v[178:181], v173 offset:21504
	ds_read_b128 v[182:185], v173 offset:22528
	ds_read_b128 v[186:189], v173 offset:23552
	s_mov_b32 m0, s55
	v_lshl_add_u64 v[42:43], s[30:31], 0, v[164:165]
	s_add_i32 s56, s55, 0x2000
	global_load_lds_dwordx4 v[42:43], off
	v_lshl_add_u64 v[42:43], s[30:31], 0, v[162:163]
	s_add_u32 s30, s2, 0x20100
	s_mov_b32 m0, s56
	s_addc_u32 s31, s3, 0
	s_add_i32 s57, s57, s33
	global_load_lds_dwordx4 v[42:43], off
	s_mov_b32 m0, s57
	v_lshl_add_u64 v[42:43], s[30:31], 0, v[164:165]
	s_add_i32 s58, s57, 0x2000
	global_load_lds_dwordx4 v[42:43], off
	v_lshl_add_u64 v[42:43], s[30:31], 0, v[162:163]
	s_mov_b32 m0, s58
	s_nop 0
	global_load_lds_dwordx4 v[42:43], off
	s_mov_b32 m0, s44
	v_lshl_add_u64 v[42:43], s[18:19], 0, v[164:165]
	global_load_lds_dwordx4 v[42:43], off
	v_lshl_add_u64 v[42:43], s[18:19], 0, v[162:163]
	s_mov_b32 m0, s45
	s_nop 0
	global_load_lds_dwordx4 v[42:43], off
	s_waitcnt vmcnt(8)
	s_waitcnt lgkmcnt(0)
	s_barrier
	s_setprio 1
	s_waitcnt lgkmcnt(0)
	v_mfma_f32_16x16x128_f8f6f4 v[102:105], v[2:9], v[34:41], 0
	v_mfma_f32_16x16x128_f8f6f4 v[98:101], v[10:17], v[34:41], 0
	v_mfma_f32_16x16x128_f8f6f4 v[78:81], v[2:9], v[50:57], 0
	v_mfma_f32_16x16x128_f8f6f4 v[74:77], v[10:17], v[50:57], 0
	v_mfma_f32_16x16x128_f8f6f4 v[62:65], v[2:9], v[174:181], 0
	v_mfma_f32_16x16x128_f8f6f4 v[58:61], v[10:17], v[174:181], 0
	v_mfma_f32_16x16x128_f8f6f4 v[46:49], v[2:9], v[182:189], 0
	v_mfma_f32_16x16x128_f8f6f4 v[42:45], v[10:17], v[182:189], 0
	s_setprio 0
	s_setprio 1
	v_mfma_f32_16x16x128_f8f6f4 v[86:89], v[18:25], v[34:41], 0
	v_mfma_f32_16x16x128_f8f6f4 v[82:85], v[26:33], v[34:41], 0
	v_mfma_f32_16x16x128_f8f6f4 v[70:73], v[18:25], v[50:57], 0
	v_mfma_f32_16x16x128_f8f6f4 v[66:69], v[26:33], v[50:57], 0
	v_mfma_f32_16x16x128_f8f6f4 v[54:57], v[18:25], v[174:181], 0
	v_mfma_f32_16x16x128_f8f6f4 v[50:53], v[26:33], v[174:181], 0
	v_mfma_f32_16x16x128_f8f6f4 v[38:41], v[18:25], v[182:189], 0
	v_mfma_f32_16x16x128_f8f6f4 v[34:37], v[26:33], v[182:189], 0
	s_setprio 0
	s_barrier
;     ...
;         PG8_TRIP(0, true);
; #pragma unroll 1
;         for (int t = 2; t < nt; t += 2) PG8_TRIP(t, false);
	s_add_i32 s40, 0, 0x18000
	s_add_i32 s59, 0, 0x1c000
	v_add_u32_e32 v168, s40, v169
	v_add_u32_e32 v170, s59, v169
	ds_read_b128 v[26:29], v168
	ds_read_b128 v[30:33], v168 offset:1024
	ds_read_b128 v[18:21], v168 offset:2048
	ds_read_b128 v[22:25], v168 offset:3072
	ds_read_b128 v[10:13], v170
	ds_read_b128 v[14:17], v170 offset:1024
	ds_read_b128 v[2:5], v170 offset:2048
	ds_read_b128 v[6:9], v170 offset:3072
	s_add_u32 s18, s6, 0x20100
	s_addc_u32 s19, s7, 0
	s_mov_b32 m0, s48
	ds_read_b128 v[174:177], v173 offset:32768
	ds_read_b128 v[178:181], v173 offset:33792
	ds_read_b128 v[182:185], v173 offset:34816
	ds_read_b128 v[186:189], v173 offset:35840
	ds_read_b128 v[194:197], v173 offset:36864
	ds_read_b128 v[198:201], v173 offset:37888
	ds_read_b128 v[214:217], v173 offset:38912
	ds_read_b128 v[218:221], v173 offset:39936
	s_nop 0
	v_lshl_add_u64 v[202:203], s[18:19], 0, v[164:165]
	global_load_lds_dwordx4 v[202:203], off
	v_lshl_add_u64 v[202:203], s[18:19], 0, v[162:163]
	s_mov_b32 m0, s49
	s_nop 0
	global_load_lds_dwordx4 v[202:203], off
	s_waitcnt vmcnt(8)
	s_waitcnt lgkmcnt(0)
	s_barrier
	s_setprio 1
	s_waitcnt lgkmcnt(0)
	v_mfma_f32_16x16x128_f8f6f4 v[154:157], v[26:33], v[174:181], v[154:157]
	v_mfma_f32_16x16x128_f8f6f4 v[158:161], v[18:25], v[174:181], v[158:161]
	v_mfma_f32_16x16x128_f8f6f4 v[138:141], v[26:33], v[182:189], v[138:141]
	v_mfma_f32_16x16x128_f8f6f4 v[130:133], v[18:25], v[182:189], v[130:133]
	v_mfma_f32_16x16x128_f8f6f4 v[126:129], v[26:33], v[194:201], v[126:129]
	v_mfma_f32_16x16x128_f8f6f4 v[122:125], v[18:25], v[194:201], v[122:125]
	v_mfma_f32_16x16x128_f8f6f4 v[110:113], v[26:33], v[214:221], v[110:113]
	v_mfma_f32_16x16x128_f8f6f4 v[106:109], v[18:25], v[214:221], v[106:109]
	s_setprio 0
	s_setprio 1
	v_mfma_f32_16x16x128_f8f6f4 v[146:149], v[10:17], v[174:181], v[146:149]
	v_mfma_f32_16x16x128_f8f6f4 v[150:153], v[2:9], v[174:181], v[150:153]
	v_mfma_f32_16x16x128_f8f6f4 v[142:145], v[10:17], v[182:189], v[142:145]
	v_mfma_f32_16x16x128_f8f6f4 v[134:137], v[2:9], v[182:189], v[134:137]
	v_mfma_f32_16x16x128_f8f6f4 v[118:121], v[10:17], v[194:201], v[118:121]
	v_mfma_f32_16x16x128_f8f6f4 v[114:117], v[2:9], v[194:201], v[114:117]
	v_mfma_f32_16x16x128_f8f6f4 v[94:97], v[10:17], v[214:221], v[94:97]
	v_mfma_f32_16x16x128_f8f6f4 v[90:93], v[2:9], v[214:221], v[90:93]
	s_setprio 0
	s_barrier
	s_add_u32 s30, s2, 0x180
	s_addc_u32 s31, s3, 0
	s_add_i32 s18, s40, s33
	ds_read_b128 v[174:177], v173 offset:49152
	ds_read_b128 v[178:181], v173 offset:50176
	ds_read_b128 v[182:185], v173 offset:51200
	ds_read_b128 v[186:189], v173 offset:52224
	ds_read_b128 v[194:197], v173 offset:53248
	ds_read_b128 v[198:201], v173 offset:54272
	ds_read_b128 v[214:217], v173 offset:55296
	ds_read_b128 v[218:221], v173 offset:56320
	s_mov_b32 m0, s18
	v_lshl_add_u64 v[202:203], s[30:31], 0, v[164:165]
	s_add_i32 s19, s18, 0x2000
	global_load_lds_dwordx4 v[202:203], off
	v_lshl_add_u64 v[202:203], s[30:31], 0, v[162:163]
	s_add_u32 s30, s2, 0x20180
	s_mov_b32 m0, s19
	s_addc_u32 s31, s3, 0
	s_add_i32 s59, s59, s33
	global_load_lds_dwordx4 v[202:203], off
	s_mov_b32 m0, s59
	v_lshl_add_u64 v[202:203], s[30:31], 0, v[164:165]
	s_add_i32 s60, s59, 0x2000
	global_load_lds_dwordx4 v[202:203], off
	v_lshl_add_u64 v[202:203], s[30:31], 0, v[162:163]
	s_mov_b32 m0, s60
	s_nop 0
	global_load_lds_dwordx4 v[202:203], off
	s_mov_b32 m0, s50
	v_lshl_add_u64 v[202:203], s[28:29], 0, v[164:165]
	global_load_lds_dwordx4 v[202:203], off
	v_lshl_add_u64 v[202:203], s[28:29], 0, v[162:163]
	s_mov_b32 m0, s51
	s_nop 0
	global_load_lds_dwordx4 v[202:203], off
	s_waitcnt vmcnt(8)
	s_waitcnt lgkmcnt(0)
	s_barrier
	s_setprio 1
	s_waitcnt lgkmcnt(0)
	v_mfma_f32_16x16x128_f8f6f4 v[102:105], v[26:33], v[174:181], v[102:105]
	v_mfma_f32_16x16x128_f8f6f4 v[98:101], v[18:25], v[174:181], v[98:101]
	v_mfma_f32_16x16x128_f8f6f4 v[78:81], v[26:33], v[182:189], v[78:81]
	v_mfma_f32_16x16x128_f8f6f4 v[74:77], v[18:25], v[182:189], v[74:77]
	v_mfma_f32_16x16x128_f8f6f4 v[62:65], v[26:33], v[194:201], v[62:65]
	v_mfma_f32_16x16x128_f8f6f4 v[58:61], v[18:25], v[194:201], v[58:61]
	v_mfma_f32_16x16x128_f8f6f4 v[46:49], v[26:33], v[214:221], v[46:49]
	v_mfma_f32_16x16x128_f8f6f4 v[42:45], v[18:25], v[214:221], v[42:45]
	s_setprio 0
	s_setprio 1
	v_mfma_f32_16x16x128_f8f6f4 v[86:89], v[10:17], v[174:181], v[86:89]
	v_mfma_f32_16x16x128_f8f6f4 v[82:85], v[2:9], v[174:181], v[82:85]
	v_mfma_f32_16x16x128_f8f6f4 v[70:73], v[10:17], v[182:189], v[70:73]
	v_mfma_f32_16x16x128_f8f6f4 v[66:69], v[2:9], v[182:189], v[66:69]
	v_mfma_f32_16x16x128_f8f6f4 v[54:57], v[10:17], v[194:201], v[54:57]
	v_mfma_f32_16x16x128_f8f6f4 v[50:53], v[2:9], v[194:201], v[50:53]
	v_mfma_f32_16x16x128_f8f6f4 v[38:41], v[10:17], v[214:221], v[38:41]
	v_mfma_f32_16x16x128_f8f6f4 v[34:37], v[2:9], v[214:221], v[34:37]
	s_setprio 0
	s_barrier
	s_mov_b32 s61, 0
	.p2align 6
